# gla_c chunk: norm-weight loads hoisted and batched (was 16 serial generic loads), row-scalar loads as global so the LDS wait does not stall the tile loads, ga rows in one wait; log1p scaffolding (deno
# baseline (speedup 1.0000x reference)
.LBB0_696:
	ds_read2st64_b32 v[14:15], v12 offset1:16
	v_add_co_u32_e32 v13, vcc, 0x200, v13
	s_xor_b64 s[30:31], vcc, -1
	s_and_b64 s[30:31], exec, s[30:31]
	s_waitcnt lgkmcnt(0)
	v_add_f32_e32 v14, v14, v15
	ds_write_b32 v12, v14
	global_store_dword v[10:11], v14, off
	v_lshl_add_u64 v[10:11], v[10:11], 0, s[12:13]
	s_or_b64 s[0:1], s[30:31], s[0:1]
	v_add_u32_e32 v12, 0x800, v12
	s_andn2_b64 exec, exec, s[0:1]
	s_cbranch_execnz .LBB0_696
	s_or_b64 exec, exec, s[0:1]
	v_cvt_pk_bf16_f32 v18, v8, v9
	s_waitcnt lgkmcnt(0)
	s_barrier
	v_lshlrev_b32_e32 v10, 16, v18
	v_and_b32_e32 v11, 0xffff0000, v18
	ds_read_b128 v[26:29], v120
	ds_read_b128 v[30:33], v120 offset:16
	v_pk_add_f32 v[8:9], v[8:9], v[10:11] neg_lo:[0,1] neg_hi:[0,1]
	v_cvt_pk_bf16_f32 v19, v6, v7
	v_cvt_pk_bf16_f32 v22, v8, v9
	v_lshlrev_b32_e32 v8, 16, v19
	v_and_b32_e32 v9, 0xffff0000, v19
	v_pk_add_f32 v[6:7], v[6:7], v[8:9] neg_lo:[0,1] neg_hi:[0,1]
	v_cvt_pk_bf16_f32 v20, v4, v5
	v_cvt_pk_bf16_f32 v23, v6, v7
	v_lshlrev_b32_e32 v6, 16, v20
	v_and_b32_e32 v7, 0xffff0000, v20
	v_pk_add_f32 v[4:5], v[4:5], v[6:7] neg_lo:[0,1] neg_hi:[0,1]
	v_cvt_pk_bf16_f32 v21, v2, v3
	s_waitcnt lgkmcnt(1)
	v_cvt_pk_bf16_f32 v34, v26, v27
	v_cvt_pk_bf16_f32 v35, v28, v29
	s_waitcnt lgkmcnt(0)
	v_cvt_pk_bf16_f32 v36, v30, v31
	v_cvt_pk_bf16_f32 v37, v32, v33
	v_cvt_pk_bf16_f32 v24, v4, v5
	v_lshlrev_b32_e32 v4, 16, v21
	v_and_b32_e32 v5, 0xffff0000, v21
	v_pk_add_f32 v[2:3], v[2:3], v[4:5] neg_lo:[0,1] neg_hi:[0,1]
	v_lshlrev_b32_e32 v38, 16, v35
	v_cvt_pk_bf16_f32 v25, v2, v3
	v_lshlrev_b32_e32 v2, 16, v34
	v_and_b32_e32 v3, 0xffff0000, v34
	v_pk_add_f32 v[2:3], v[26:27], v[2:3] neg_lo:[0,1] neg_hi:[0,1]
	v_and_b32_e32 v39, 0xffff0000, v35
	v_cvt_pk_bf16_f32 v26, v2, v3
	v_mfma_f32_32x32x16_bf16 v[2:17], v[34:37], v[18:21], 0
	v_add_f32_e64 v28, v28, -v38
	v_add_f32_e64 v29, v29, -v39
	ds_read_b128 v[38:41], v120 offset:2048
	v_cvt_pk_bf16_f32 v27, v28, v29
	v_lshlrev_b32_e32 v28, 16, v36
	v_and_b32_e32 v29, 0xffff0000, v36
	v_pk_add_f32 v[28:29], v[30:31], v[28:29] neg_lo:[0,1] neg_hi:[0,1]
	v_lshlrev_b32_e32 v30, 16, v37
	v_mfma_f32_32x32x16_bf16 v[2:17], v[34:37], v[22:25], v[2:17]
	v_and_b32_e32 v31, 0xffff0000, v37
	v_add_f32_e64 v30, v32, -v30
	v_add_f32_e64 v31, v33, -v31
	v_cvt_pk_bf16_f32 v28, v28, v29
	v_cvt_pk_bf16_f32 v29, v30, v31
	s_nop 1
	v_mfma_f32_32x32x16_bf16 v[2:17], v[26:29], v[18:21], v[2:17]
	s_nop 11
	v_add_f32_e32 v2, v46, v2
	v_mul_f32_e64 v26, |v2|, s26
	v_exp_f32_e32 v26, v26
	v_add_f32_e32 v3, v46, v3
	v_mul_f32_e64 v28, |v3|, s26
	v_exp_f32_e32 v28, v28
	v_add_f32_e32 v26, 1.0, v26
	v_add_f32_e32 v29, v46, v4
	v_mul_f32_e64 v4, |v29|, s26
	v_log_f32_e32 v26, v26
	v_exp_f32_e32 v4, v4
	v_add_f32_e32 v5, v46, v5
	v_mul_f32_e64 v30, |v5|, s26
	v_mul_f32_e32 v27, 0x3f317217, v26
	v_fma_f32 v27, v26, s28, -v27
	v_fmac_f32_e32 v27, 0x3377d1cf, v26
	v_fmac_f32_e32 v27, 0x3f317217, v26
	v_add_f32_e32 v4, 1.0, v4
	v_exp_f32_e32 v30, v30
	v_mov_b32_e32 v26, v27
	v_add_f32_e32 v27, 1.0, v28
	v_add_f32_e32 v6, v46, v6
	v_mul_f32_e64 v31, |v6|, s26
	v_log_f32_e32 v27, v27
	v_mov_b32_e32 v28, v26
	v_min_f32_e32 v26, 0, v3
	v_mul_f32_e32 v3, 0x3f317217, v27
	v_fma_f32 v3, v27, s28, -v3
	v_fmac_f32_e32 v3, 0x3377d1cf, v27
	v_fmac_f32_e32 v3, 0x3f317217, v27
	v_exp_f32_e32 v31, v31
	v_add_f32_e32 v7, v46, v7
	v_mul_f32_e64 v32, |v7|, s26
	v_exp_f32_e32 v32, v32
	v_log_f32_e32 v27, v4
	v_mov_b32_e32 v4, v3
	v_min_f32_e32 v3, 0, v29
	v_mul_f32_e32 v29, 0x3f317217, v27
	v_fma_f32 v29, v27, s28, -v29
	v_fmac_f32_e32 v29, 0x3377d1cf, v27
	v_fmac_f32_e32 v29, 0x3f317217, v27
	v_min_f32_e32 v34, 0, v7
	v_add_f32_e32 v9, v46, v9
	v_mov_b32_e32 v27, v29
	v_add_f32_e32 v29, 1.0, v30
	v_mul_f32_e64 v33, |v9|, s26
	v_exp_f32_e32 v33, v33
	v_log_f32_e32 v30, v29
	v_mov_b32_e32 v29, v27
	v_min_f32_e32 v27, 0, v5
	v_mul_f32_e32 v5, 0x3f317217, v30
	v_fma_f32 v5, v30, s28, -v5
	v_fmac_f32_e32 v5, 0x3377d1cf, v30
	v_fmac_f32_e32 v5, 0x3f317217, v30
	v_add_f32_e32 v10, v46, v10
	v_min_f32_e32 v35, 0, v9
	v_add_f32_e32 v30, 1.0, v31
	v_add_f32_e32 v11, v46, v11
	v_mul_f32_e64 v36, |v11|, s26
	v_log_f32_e32 v30, v30
	v_exp_f32_e32 v36, v36
	v_mul_f32_e32 v31, 0x3f317217, v30
	v_fma_f32 v31, v30, s28, -v31
	v_fmac_f32_e32 v31, 0x3377d1cf, v30
	v_fmac_f32_e32 v31, 0x3f317217, v30
	v_add_f32_e32 v12, v46, v12
	v_add_f32_e32 v13, v46, v13
	v_mov_b32_e32 v30, v31
	v_add_f32_e32 v31, 1.0, v32
	v_min_f32_e32 v37, 0, v13
	v_min_f32_e32 v2, 0, v2
	v_log_f32_e32 v31, v31
	v_mov_b32_e32 v32, v30
	v_add_f32_e32 v30, v46, v8
	v_mul_f32_e64 v8, |v30|, s26
	v_exp_f32_e32 v8, v8
	v_mul_f32_e32 v7, 0x3f317217, v31
	v_fma_f32 v7, v31, s28, -v7
	v_fmac_f32_e32 v7, 0x3377d1cf, v31
	v_fmac_f32_e32 v7, 0x3f317217, v31
	v_add_f32_e32 v8, 1.0, v8
	v_min_f32_e32 v6, 0, v6
	s_nop 1
	v_log_f32_e32 v31, v8
	v_mov_b32_e32 v8, v7
	v_min_f32_e32 v7, 0, v30
	v_mul_f32_e32 v30, 0x3f317217, v31
	v_fma_f32 v30, v31, s28, -v30
	v_fmac_f32_e32 v30, 0x3377d1cf, v31
	v_fmac_f32_e32 v30, 0x3f317217, v31
	s_nop 1
	v_add_f32_e32 v31, 1.0, v33
	s_nop 1
	v_log_f32_e32 v31, v31
	v_mov_b32_e32 v33, v30
	v_mul_f32_e64 v30, |v10|, s26
	v_exp_f32_e32 v30, v30
	v_mul_f32_e32 v9, 0x3f317217, v31
	v_fma_f32 v9, v31, s28, -v9
	v_fmac_f32_e32 v9, 0x3377d1cf, v31
	v_fmac_f32_e32 v9, 0x3f317217, v31
	v_add_f32_e32 v30, 1.0, v30
	v_min_f32_e32 v10, 0, v10
	v_pk_add_f32 v[32:33], v[6:7], v[32:33] neg_lo:[0,1] neg_hi:[0,1]
	s_nop 0
	v_log_f32_e32 v30, v30
	s_nop 0
	v_mul_f32_e32 v31, 0x3f317217, v30
	v_fma_f32 v31, v30, s28, -v31
	v_fmac_f32_e32 v31, 0x3377d1cf, v30
	v_fmac_f32_e32 v31, 0x3f317217, v30
	s_nop 1
	v_mov_b32_e32 v30, v31
	v_add_f32_e32 v31, 1.0, v36
	s_nop 1
	v_log_f32_e32 v31, v31
	v_mov_b32_e32 v42, v30
	v_mul_f32_e64 v30, |v12|, s26
	v_exp_f32_e32 v30, v30
	v_min_f32_e32 v36, 0, v11
	v_mul_f32_e32 v11, 0x3f317217, v31
	v_fma_f32 v11, v31, s28, -v11
	v_fmac_f32_e32 v11, 0x3377d1cf, v31
	v_fmac_f32_e32 v11, 0x3f317217, v31
	v_add_f32_e32 v30, 1.0, v30
	s_nop 0
	s_nop 1
	v_log_f32_e32 v30, v30
	v_mov_b32_e32 v54, v11
	v_mul_f32_e64 v31, |v13|, s26
	v_min_f32_e32 v11, 0, v12
	v_mul_f32_e32 v12, 0x3f317217, v30
	v_exp_f32_e32 v31, v31
	v_fma_f32 v12, v30, s28, -v12
	v_fmac_f32_e32 v12, 0x3377d1cf, v30
	v_fmac_f32_e32 v12, 0x3f317217, v30
	v_add_f32_e32 v13, v46, v14
	v_mul_f32_e64 v14, |v13|, s26
	v_add_f32_e32 v30, 1.0, v31
	v_exp_f32_e32 v14, v14
	v_min_f32_e32 v56, 0, v13
	v_log_f32_e32 v30, v30
	v_mov_b32_e32 v43, v12
	v_add_f32_e32 v14, 1.0, v14
	v_mul_f32_e32 v12, 0x3f317217, v30
	v_fma_f32 v12, v30, s28, -v12
	v_fmac_f32_e32 v12, 0x3377d1cf, v30
	v_fmac_f32_e32 v12, 0x3f317217, v30
	v_add_f32_e32 v13, v46, v15
	v_mul_f32_e64 v15, |v13|, s26
	v_exp_f32_e32 v15, v15
	v_min_f32_e32 v60, 0, v13
	v_log_f32_e32 v14, v14
	v_mov_b32_e32 v55, v12
	v_add_f32_e32 v13, v46, v16
	v_mul_f32_e32 v12, 0x3f317217, v14
	v_fma_f32 v12, v14, s28, -v12
	v_fmac_f32_e32 v12, 0x3377d1cf, v14
	v_fmac_f32_e32 v12, 0x3f317217, v14
	v_min_f32_e32 v57, 0, v13
	v_pk_add_f32 v[30:31], v[2:3], v[28:29] neg_lo:[0,1] neg_hi:[0,1]
	v_add_f32_e32 v14, 1.0, v15
	v_pk_add_f32 v[2:3], v[26:27], v[4:5] neg_lo:[0,1] neg_hi:[0,1]
	s_nop 0
	v_log_f32_e32 v14, v14
	v_mov_b32_e32 v58, v12
	v_mul_f32_e64 v15, |v13|, s26
	v_mul_f32_e32 v12, 0x3f317217, v14
	v_exp_f32_e32 v15, v15
	v_fma_f32 v12, v14, s28, -v12
	v_fmac_f32_e32 v12, 0x3377d1cf, v14
	v_fmac_f32_e32 v12, 0x3f317217, v14
	v_add_f32_e32 v13, v46, v17
	v_pk_mul_f32 v[26:27], v[2:3], s[14:15] op_sel_hi:[1,0]
	v_add_f32_e32 v14, 1.0, v15
	v_pk_fma_f32 v[2:3], v[30:31], s[14:15], v[26:27] op_sel_hi:[1,0,1]
	v_min_f32_e32 v61, 0, v13
	v_log_f32_e32 v14, v14
	v_mov_b32_e32 v62, v12
	v_mul_f32_e64 v15, |v13|, s26
	v_mul_f32_e32 v12, 0x3f317217, v14
	v_exp_f32_e32 v15, v15
	v_fma_f32 v12, v14, s28, -v12
	v_fmac_f32_e32 v12, 0x3377d1cf, v14
	v_fmac_f32_e32 v12, 0x3f317217, v14
	v_add_f32_e32 v47, v2, v3
	v_pk_add_f32 v[2:3], v[34:35], v[8:9] neg_lo:[0,1] neg_hi:[0,1]
	v_add_f32_e32 v14, 1.0, v15
	v_pk_add_f32 v[34:35], v[10:11], v[42:43] neg_lo:[0,1] neg_hi:[0,1]
	ds_read_b128 v[42:45], v120 offset:2064
	v_log_f32_e32 v14, v14
	v_mov_b32_e32 v59, v12
	s_waitcnt lgkmcnt(1)
	v_cvt_pk_bf16_f32 v50, v38, v39
	v_mul_f32_e32 v12, 0x3f317217, v14
	v_cvt_pk_bf16_f32 v51, v40, v41
	s_waitcnt lgkmcnt(0)
	v_cvt_pk_bf16_f32 v52, v42, v43
	v_cvt_pk_bf16_f32 v53, v44, v45
	v_fma_f32 v12, v14, s28, -v12
	v_pk_mul_f32 v[28:29], v[2:3], s[14:15] op_sel_hi:[1,0]
	v_fmac_f32_e32 v12, 0x3377d1cf, v14
	v_pk_fma_f32 v[2:3], v[32:33], s[14:15], v[28:29] op_sel_hi:[1,0,1]
	v_fmac_f32_e32 v12, 0x3f317217, v14
	v_add_f32_e32 v48, v2, v3
	v_lshlrev_b32_e32 v2, 16, v50
	v_and_b32_e32 v3, 0xffff0000, v50
	v_pk_add_f32 v[2:3], v[38:39], v[2:3] neg_lo:[0,1] neg_hi:[0,1]
	v_mov_b32_e32 v63, v12
	v_cvt_pk_bf16_f32 v38, v2, v3
	v_mfma_f32_32x32x16_bf16 v[2:17], v[50:53], v[18:21], 0
	v_lshlrev_b32_e32 v64, 16, v51
	v_and_b32_e32 v65, 0xffff0000, v51
	v_add_f32_e64 v40, v40, -v64
	v_add_f32_e64 v41, v41, -v65
	v_cvt_pk_bf16_f32 v39, v40, v41
	v_lshlrev_b32_e32 v40, 16, v52
	v_and_b32_e32 v41, 0xffff0000, v52
	v_mfma_f32_32x32x16_bf16 v[2:17], v[50:53], v[22:25], v[2:17]
	v_add_f32_e64 v40, v42, -v40
	v_add_f32_e64 v41, v43, -v41
	v_lshlrev_b32_e32 v42, 16, v53
	v_and_b32_e32 v43, 0xffff0000, v53
	v_add_f32_e64 v22, v44, -v42
	v_add_f32_e64 v23, v45, -v43
	v_cvt_pk_bf16_f32 v40, v40, v41
	v_cvt_pk_bf16_f32 v41, v22, v23
	v_pk_add_f32 v[22:23], v[36:37], v[54:55] neg_lo:[0,1] neg_hi:[0,1]
	s_nop 0
	v_mfma_f32_32x32x16_bf16 v[2:17], v[38:41], v[18:21], v[2:17]
	v_mul_f32_e64 v22, v22, s14
	v_mul_f32_e64 v23, v23, s14
	v_add_f32_e64 v20, v56, -v58
	v_add_f32_e64 v21, v57, -v59
	v_fma_f32 v24, v34, s14, v22
	v_fma_f32 v25, v35, s14, v23
	s_nop 5
	v_add_f32_e32 v2, v46, v2
	v_pk_add_f32 v[24:25], v[24:25], v[24:25] op_sel:[0,1] op_sel_hi:[1,0]
	v_mul_f32_e64 v18, |v2|, s26
	v_exp_f32_e32 v25, v18
	v_pk_add_f32 v[18:19], v[60:61], v[62:63] neg_lo:[0,1] neg_hi:[0,1]
	v_add_f32_e32 v3, v46, v3
	v_pk_mul_f32 v[18:19], v[18:19], s[14:15] op_sel_hi:[1,0]
	v_add_f32_e32 v25, 1.0, v25
	v_mul_f32_e64 v38, |v3|, s26
	v_exp_f32_e32 v38, v38
	v_log_f32_e32 v25, v25
	v_pk_fma_f32 v[36:37], v[20:21], s[14:15], v[18:19] op_sel_hi:[1,0,1]
	v_add_f32_e32 v5, v46, v5
	v_pk_add_f32 v[36:37], v[36:37], v[36:37] op_sel:[0,1] op_sel_hi:[1,0]
	v_mul_f32_e32 v37, 0x3f317217, v25
	v_fma_f32 v37, v25, s28, -v37
	v_fmac_f32_e32 v37, 0x3377d1cf, v25
	v_fmac_f32_e32 v37, 0x3f317217, v25
	v_mov_b32_e32 v25, v37
	v_add_f32_e32 v37, 1.0, v38
	v_mul_f32_e64 v39, |v5|, s26
	v_exp_f32_e32 v39, v39
	v_log_f32_e32 v37, v37
	v_mov_b32_e32 v40, v25
	v_add_f32_e32 v25, v46, v4
	v_mul_f32_e64 v4, |v25|, s26
	v_exp_f32_e32 v4, v4
	v_min_f32_e32 v38, 0, v3
	v_mul_f32_e32 v3, 0x3f317217, v37
	v_fma_f32 v3, v37, s28, -v3
	v_fmac_f32_e32 v3, 0x3377d1cf, v37
	v_fmac_f32_e32 v3, 0x3f317217, v37
	v_add_f32_e32 v4, 1.0, v4
	v_add_f32_e32 v6, v46, v6
	v_add_f32_e32 v7, v46, v7
	v_mul_f32_e64 v42, |v7|, s26
	v_log_f32_e32 v37, v4
	v_mov_b32_e32 v4, v3
	v_min_f32_e32 v3, 0, v25
	v_mul_f32_e32 v25, 0x3f317217, v37
	v_fma_f32 v25, v37, s28, -v25
	v_fmac_f32_e32 v25, 0x3377d1cf, v37
	v_fmac_f32_e32 v25, 0x3f317217, v37
	v_exp_f32_e32 v42, v42
	v_add_f32_e32 v9, v46, v9
	v_add_f32_e32 v37, 1.0, v39
	v_mul_f32_e64 v43, |v9|, s26
	v_exp_f32_e32 v43, v43
	v_log_f32_e32 v37, v37
	v_mov_b32_e32 v41, v25
	v_mul_f32_e64 v25, |v6|, s26
	v_exp_f32_e32 v25, v25
	v_min_f32_e32 v39, 0, v5
	v_mul_f32_e32 v5, 0x3f317217, v37
	v_fma_f32 v5, v37, s28, -v5
	v_fmac_f32_e32 v5, 0x3377d1cf, v37
	v_fmac_f32_e32 v5, 0x3f317217, v37
	v_add_f32_e32 v25, 1.0, v25
	v_add_f32_e32 v10, v46, v10
	v_add_f32_e32 v11, v46, v11
	v_min_f32_e32 v50, 0, v10
	v_log_f32_e32 v25, v25
	v_min_f32_e32 v54, 0, v11
	v_mul_f32_e32 v37, 0x3f317217, v25
	v_fma_f32 v37, v25, s28, -v37
	v_fmac_f32_e32 v37, 0x3377d1cf, v25
	v_fmac_f32_e32 v37, 0x3f317217, v25
	v_min_f32_e32 v2, 0, v2
	v_min_f32_e32 v6, 0, v6
	v_mov_b32_e32 v25, v37
	v_add_f32_e32 v37, 1.0, v42
	s_nop 1
	v_log_f32_e32 v37, v37
	v_mov_b32_e32 v44, v25
	v_add_f32_e32 v25, v46, v8
	v_mul_f32_e64 v8, |v25|, s26
	v_exp_f32_e32 v8, v8
	v_min_f32_e32 v42, 0, v7
	v_mul_f32_e32 v7, 0x3f317217, v37
	v_fma_f32 v7, v37, s28, -v7
	v_fmac_f32_e32 v7, 0x3377d1cf, v37
	v_fmac_f32_e32 v7, 0x3f317217, v37
	v_add_f32_e32 v8, 1.0, v8
	s_nop 0
	s_nop 1
	v_log_f32_e32 v37, v8
	v_mov_b32_e32 v8, v7
	v_min_f32_e32 v7, 0, v25
	v_mul_f32_e32 v25, 0x3f317217, v37
	v_fma_f32 v25, v37, s28, -v25
	v_fmac_f32_e32 v25, 0x3377d1cf, v37
	v_fmac_f32_e32 v25, 0x3f317217, v37
	s_nop 1
	v_add_f32_e32 v37, 1.0, v43
	s_nop 1
	v_log_f32_e32 v37, v37
	v_mov_b32_e32 v45, v25
	v_mul_f32_e64 v25, |v10|, s26
	v_exp_f32_e32 v25, v25
	v_min_f32_e32 v43, 0, v9
	v_mul_f32_e32 v9, 0x3f317217, v37
	v_fma_f32 v9, v37, s28, -v9
	v_fmac_f32_e32 v9, 0x3377d1cf, v37
	v_fmac_f32_e32 v9, 0x3f317217, v37
	v_add_f32_e32 v25, 1.0, v25
	v_pk_add_f32 v[6:7], v[6:7], v[44:45] neg_lo:[0,1] neg_hi:[0,1]
	s_nop 1
	v_log_f32_e32 v25, v25
	v_mul_f32_e64 v37, |v11|, s26
	v_mul_f32_e32 v10, 0x3f317217, v25
	v_exp_f32_e32 v37, v37
	v_fma_f32 v10, v25, s28, -v10
	v_fmac_f32_e32 v10, 0x3377d1cf, v25
	v_fmac_f32_e32 v10, 0x3f317217, v25
	v_add_f32_e32 v11, v46, v12
	v_mul_f32_e64 v12, |v11|, s26
	v_add_f32_e32 v25, 1.0, v37
	v_exp_f32_e32 v12, v12
	v_min_f32_e32 v51, 0, v11
	v_log_f32_e32 v25, v25
	v_mov_b32_e32 v52, v10
	v_add_f32_e32 v12, 1.0, v12
	v_mul_f32_e32 v10, 0x3f317217, v25
	v_fma_f32 v10, v25, s28, -v10
	v_fmac_f32_e32 v10, 0x3377d1cf, v25
	v_fmac_f32_e32 v10, 0x3f317217, v25
	v_add_f32_e32 v11, v46, v13
	v_mul_f32_e64 v13, |v11|, s26
	v_exp_f32_e32 v13, v13
	v_min_f32_e32 v55, 0, v11
	v_log_f32_e32 v12, v12
	v_mov_b32_e32 v56, v10
	v_add_f32_e32 v11, v46, v14
	v_mul_f32_e32 v10, 0x3f317217, v12
	v_fma_f32 v10, v12, s28, -v10
	v_fmac_f32_e32 v10, 0x3377d1cf, v12
	v_fmac_f32_e32 v10, 0x3f317217, v12
	v_min_f32_e32 v14, 0, v11
	v_and_b32_e32 v37, 64, v140
	v_add_f32_e32 v12, 1.0, v13
	v_xor_b32_e32 v25, 32, v140
	v_add_u32_e32 v37, 64, v37
	v_log_f32_e32 v12, v12
	v_mov_b32_e32 v53, v10
	v_mul_f32_e64 v13, |v11|, s26
	v_mul_f32_e32 v10, 0x3f317217, v12
	v_exp_f32_e32 v13, v13
	v_fma_f32 v10, v12, s28, -v10
	v_fmac_f32_e32 v10, 0x3377d1cf, v12
	v_fmac_f32_e32 v10, 0x3f317217, v12
	v_add_f32_e32 v11, v46, v15
	v_min_f32_e32 v60, 0, v11
	v_add_f32_e32 v12, 1.0, v13
	s_nop 1
	v_log_f32_e32 v12, v12
	v_mov_b32_e32 v57, v10
	v_mul_f32_e64 v13, |v11|, s26
	v_mul_f32_e32 v10, 0x3f317217, v12
	v_exp_f32_e32 v13, v13
	v_fma_f32 v10, v12, s28, -v10
	v_fmac_f32_e32 v10, 0x3377d1cf, v12
	v_fmac_f32_e32 v10, 0x3f317217, v12
	v_add_f32_e32 v11, v46, v16
	v_min_f32_e32 v15, 0, v11
	v_add_f32_e32 v12, 1.0, v13
	s_nop 1
	v_log_f32_e32 v12, v12
	v_mov_b32_e32 v58, v10
	v_mul_f32_e64 v13, |v11|, s26
	v_mul_f32_e32 v10, 0x3f317217, v12
	v_exp_f32_e32 v13, v13
	v_fma_f32 v10, v12, s28, -v10
	v_fmac_f32_e32 v10, 0x3377d1cf, v12
	v_fmac_f32_e32 v10, 0x3f317217, v12
	v_add_f32_e32 v11, v46, v17
	v_min_f32_e32 v61, 0, v11
	v_add_f32_e32 v12, 1.0, v13
	s_nop 1
	v_log_f32_e32 v12, v12
	v_mov_b32_e32 v16, v10
	v_mul_f32_e64 v13, |v11|, s26
	v_mul_f32_e32 v10, 0x3f317217, v12
	v_exp_f32_e32 v13, v13
	v_fma_f32 v10, v12, s28, -v10
	v_fmac_f32_e32 v10, 0x3377d1cf, v12
	v_fmac_f32_e32 v10, 0x3f317217, v12
	s_nop 1
	v_add_f32_e32 v12, 1.0, v13
	s_nop 1
	v_log_f32_e32 v12, v12
	v_mov_b32_e32 v59, v10
	v_mul_f32_e32 v10, 0x3f317217, v12
	v_fma_f32 v10, v12, s28, -v10
	v_fmac_f32_e32 v10, 0x3377d1cf, v12
	v_fmac_f32_e32 v10, 0x3f317217, v12
	v_pk_add_f32 v[14:15], v[14:15], v[58:59] neg_lo:[0,1] neg_hi:[0,1]
	s_nop 0
	v_mov_b32_e32 v17, v10
	v_pk_add_f32 v[10:11], v[2:3], v[40:41] neg_lo:[0,1] neg_hi:[0,1]
	v_pk_add_f32 v[2:3], v[38:39], v[4:5] neg_lo:[0,1] neg_hi:[0,1]
	v_cmp_lt_i32_e32 vcc, v25, v37
	v_pk_mul_f32 v[2:3], v[2:3], s[14:15] op_sel_hi:[1,0]
	v_pk_add_f32 v[12:13], v[50:51], v[52:53] neg_lo:[0,1] neg_hi:[0,1]
	v_pk_fma_f32 v[4:5], v[10:11], s[14:15], v[2:3] op_sel_hi:[1,0,1]
	v_pk_add_f32 v[16:17], v[60:61], v[16:17] neg_lo:[0,1] neg_hi:[0,1]
	v_pk_add_f32 v[62:63], v[4:5], v[4:5] op_sel:[0,1] op_sel_hi:[1,0]
	v_pk_add_f32 v[4:5], v[42:43], v[8:9] neg_lo:[0,1] neg_hi:[0,1]
	v_cndmask_b32_e32 v25, v140, v25, vcc
	v_pk_mul_f32 v[4:5], v[4:5], s[14:15] op_sel_hi:[1,0]
	v_lshlrev_b32_e32 v45, 2, v25
	v_pk_fma_f32 v[8:9], v[6:7], s[14:15], v[4:5] op_sel_hi:[1,0,1]
	v_pk_mul_f32 v[16:17], v[16:17], s[14:15] op_sel_hi:[1,0]
	v_pk_add_f32 v[64:65], v[8:9], v[8:9] op_sel:[0,1] op_sel_hi:[1,0]
	v_pk_add_f32 v[8:9], v[54:55], v[56:57] neg_lo:[0,1] neg_hi:[0,1]
	ds_bpermute_b32 v25, v45, v47
	v_pk_mul_f32 v[8:9], v[8:9], s[14:15] op_sel_hi:[1,0]
	ds_bpermute_b32 v41, v45, v24
	v_pk_fma_f32 v[38:39], v[12:13], s[14:15], v[8:9] op_sel_hi:[1,0,1]
	ds_bpermute_b32 v42, v45, v36
	v_pk_add_f32 v[50:51], v[38:39], v[38:39] op_sel:[0,1] op_sel_hi:[1,0]
	v_pk_fma_f32 v[38:39], v[14:15], s[14:15], v[16:17] op_sel_hi:[1,0,1]
	ds_bpermute_b32 v44, v45, v62
	v_pk_add_f32 v[52:53], v[38:39], v[38:39] op_sel:[0,1] op_sel_hi:[1,0]
	ds_bpermute_b32 v38, v45, v48
	s_waitcnt lgkmcnt(4)
	v_add_f32_e32 v37, 0, v25
	v_add_f32_e32 v25, v47, v25
	ds_bpermute_b32 v46, v45, v64
	v_add_f32_e32 v25, 0, v25
	s_waitcnt lgkmcnt(1)
	v_add_f32_e32 v39, v48, v38
	ds_bpermute_b32 v48, v45, v50
	v_add_f32_e32 v39, v39, v25
	v_add_f32_e32 v24, v24, v41
	ds_bpermute_b32 v49, v45, v52
	v_add_f32_e32 v40, v24, v39
	v_add_f32_e32 v24, v36, v42
	v_add_f32_e32 v36, v24, v40
	v_add_f32_e32 v24, v62, v44
	v_add_f32_e32 v43, v36, v24
	s_waitcnt lgkmcnt(2)
	v_add_f32_e32 v24, v64, v46
	v_add_f32_e32 v45, v24, v43
	s_waitcnt lgkmcnt(1)
	v_add_f32_e32 v24, v50, v48
	v_add_f32_e32 v47, v24, v45
	s_waitcnt lgkmcnt(0)
	v_add_f32_e32 v24, v52, v49
	v_add_f32_e32 v24, v24, v47
	s_and_saveexec_b64 s[0:1], s[4:5]
	s_cbranch_execz .LBB0_694
	v_mul_f32_e32 v37, 0x3fb8aa3b, v24
	v_exp_f32_e32 v37, v37
	v_lshl_add_u32 v48, s16, 8, v66
	v_ashrrev_i32_e32 v49, 31, v48
	v_lshl_add_u64 v[48:49], v[48:49], 2, s[8:9]
	global_store_dword v[48:49], v37, off
	v_mov_b32_e32 v38, 0
	v_mov_b32_e32 v37, 0
	v_mov_b32_e32 v49, 0
	v_mov_b32_e32 v48, 0
	v_mov_b32_e32 v46, 0
	v_mov_b32_e32 v44, 0
	v_mov_b32_e32 v42, 0
	v_mov_b32_e32 v41, 0
	s_branch .LBB0_694

.LBB0_1053:
	s_nop 0
	s_nop 0
	s_nop 0
	v_and_b32_e32 v3, 64, v68
	v_xor_b32_e32 v2, 32, v68
	v_add_u32_e32 v3, 64, v3
	v_cmp_lt_i32_e32 vcc, v2, v3
	s_mov_b64 s[20:21], -1
	s_mov_b64 s[22:23], -1
	v_cndmask_b32_e32 v2, v68, v2, vcc
	v_lshlrev_b32_e32 v2, 2, v2
	ds_bpermute_b32 v6, v2, v71
	ds_bpermute_b32 v5, v2, v50
	ds_bpermute_b32 v3, v2, v57
	ds_bpermute_b32 v7, v2, v69
	ds_bpermute_b32 v4, v2, v59
	ds_bpermute_b32 v2, v2, v70
	s_waitcnt lgkmcnt(5)
	v_cmp_nlt_f32_e32 vcc, v71, v6
	s_and_saveexec_b64 s[18:19], vcc
	s_cbranch_execz .LBB0_1057
	v_cmp_eq_f32_e32 vcc, v71, v6
	s_mov_b64 s[22:23], 0
	s_and_saveexec_b64 s[24:25], vcc
	s_cbranch_execz .LBB0_1056
	s_waitcnt lgkmcnt(2)
	v_cmp_lt_i32_e32 vcc, v7, v69
	s_and_b64 s[22:23], vcc, exec

.LBB0_1411:
	v_mov_b32_e32 v66, s54
	v_mov_b32_e32 v67, s55
	ds_read_b32 v66, v66
	ds_read_b32 v67, v67
	s_waitcnt lgkmcnt(0)
	s_barrier
	s_waitcnt lgkmcnt(1)
	v_readfirstlane_b32 s0, v66
	s_waitcnt lgkmcnt(0)
	v_readfirstlane_b32 s1, v67
	v_mul_f32_e32 v80, v51, v51
	v_fmac_f32_e32 v80, v50, v50
	v_lshl_add_u64 v[68:69], s[0:1], 0, v[134:135]
	global_load_dwordx4 v[70:73], v[68:69], off
	global_load_dwordx4 v[114:117], v[68:69], off offset:32
	global_load_dwordx4 v[118:121], v[68:69], off offset:64
	global_load_dwordx4 v[122:125], v[68:69], off offset:96
	global_load_dwordx4 v[126:129], v[68:69], off offset:128
	global_load_dwordx4 v[208:211], v[68:69], off offset:160
	global_load_dwordx4 v[212:215], v[68:69], off offset:192
	global_load_dwordx4 v[232:235], v[68:69], off offset:224
	global_load_dwordx4 v[236:239], v[68:69], off offset:256
	global_load_dwordx4 v[240:243], v[68:69], off offset:288
	global_load_dwordx4 v[244:247], v[68:69], off offset:320
	global_load_dwordx4 v[248:251], v[68:69], off offset:384
	v_fmac_f32_e32 v80, v52, v52
	v_fmac_f32_e32 v80, v53, v53
	v_fmac_f32_e32 v80, v54, v54
	v_fmac_f32_e32 v80, v55, v55
	v_fmac_f32_e32 v80, v56, v56
	v_fmac_f32_e32 v80, v57, v57
	v_fmac_f32_e32 v80, v58, v58
	v_fmac_f32_e32 v80, v59, v59
	v_fmac_f32_e32 v80, v60, v60
	v_fmac_f32_e32 v80, v61, v61
	v_fmac_f32_e32 v80, v62, v62
	v_fmac_f32_e32 v80, v63, v63
	v_fmac_f32_e32 v80, v64, v64
	v_fmac_f32_e32 v80, v65, v65
	v_fmac_f32_e32 v80, v34, v34
	v_fmac_f32_e32 v80, v35, v35
	v_fmac_f32_e32 v80, v36, v36
	v_fmac_f32_e32 v80, v37, v37
	v_fmac_f32_e32 v80, v38, v38
	v_fmac_f32_e32 v80, v39, v39
	v_fmac_f32_e32 v80, v40, v40
	v_fmac_f32_e32 v80, v41, v41
	v_fmac_f32_e32 v80, v42, v42
	v_fmac_f32_e32 v80, v43, v43
	v_fmac_f32_e32 v80, v44, v44
	v_fmac_f32_e32 v80, v45, v45
	v_fmac_f32_e32 v80, v46, v46
	v_fmac_f32_e32 v80, v47, v47
	v_fmac_f32_e32 v80, v48, v48
	v_fmac_f32_e32 v80, v49, v49
	v_fmac_f32_e32 v80, v18, v18
	v_fmac_f32_e32 v80, v19, v19
	v_fmac_f32_e32 v80, v20, v20
	v_fmac_f32_e32 v80, v21, v21
	v_fmac_f32_e32 v80, v22, v22
	v_fmac_f32_e32 v80, v23, v23
	v_fmac_f32_e32 v80, v24, v24
	v_fmac_f32_e32 v80, v25, v25
	v_fmac_f32_e32 v80, v26, v26
	v_fmac_f32_e32 v80, v27, v27
	v_fmac_f32_e32 v80, v28, v28
	v_fmac_f32_e32 v80, v29, v29
	v_fmac_f32_e32 v80, v30, v30
	v_fmac_f32_e32 v80, v31, v31
	v_fmac_f32_e32 v80, v32, v32
	v_fmac_f32_e32 v80, v33, v33
	v_fmac_f32_e32 v80, v2, v2
	v_fmac_f32_e32 v80, v3, v3
	v_fmac_f32_e32 v80, v4, v4
	v_fmac_f32_e32 v80, v5, v5
	v_fmac_f32_e32 v80, v6, v6
	v_fmac_f32_e32 v80, v7, v7
	v_fmac_f32_e32 v80, v8, v8
	v_fmac_f32_e32 v80, v9, v9
	v_pk_mul_f32 v[78:79], v[10:11], v[10:11]
	v_pk_mul_f32 v[76:77], v[12:13], v[12:13]
	v_add_f32_e32 v78, v78, v80
	v_add_f32_e32 v78, v79, v78
	v_add_f32_e32 v76, v76, v78
	v_pk_mul_f32 v[74:75], v[14:15], v[14:15]
	v_add_f32_e32 v76, v77, v76
	v_add_f32_e32 v74, v74, v76
	v_pk_mul_f32 v[66:67], v[16:17], v[16:17]
	v_add_f32_e32 v74, v75, v74
	v_add_f32_e32 v66, v66, v74
	v_add_f32_e32 v66, v67, v66
	ds_bpermute_b32 v67, v1, v66
	s_waitcnt vmcnt(0)
	v_lshlrev_b32_e32 v76, 16, v91
	v_and_b32_e32 v77, 0xffff0000, v91
	v_lshlrev_b32_e32 v78, 16, v92
	v_and_b32_e32 v79, 0xffff0000, v92
	s_waitcnt lgkmcnt(0)
	v_add_f32_e32 v66, v66, v67
	v_mov_b32_e32 v67, 0x358637bd
	v_fmamk_f32 v66, v66, 0x3c000000, v67
	v_rsq_f32_e32 v66, v66
	v_add_u32_e32 v67, v189, v190
	v_lshlrev_b32_e32 v80, 16, v93
	v_and_b32_e32 v81, 0xffff0000, v93
	v_pk_mul_f32 v[50:51], v[50:51], v[66:67] op_sel_hi:[1,0]
	v_pk_mul_f32 v[52:53], v[52:53], v[66:67] op_sel_hi:[1,0]
	v_pk_mul_f32 v[50:51], v[50:51], v[70:71]
	v_pk_mul_f32 v[52:53], v[52:53], v[72:73]
	v_cvt_pk_bf16_f32 v50, v50, v51
	v_cvt_pk_bf16_f32 v51, v52, v53
	ds_write_b64 v67, v[50:51]
	v_pk_mul_f32 v[54:55], v[54:55], v[66:67] op_sel_hi:[1,0]
	v_pk_mul_f32 v[56:57], v[56:57], v[66:67] op_sel_hi:[1,0]
	v_pk_mul_f32 v[54:55], v[54:55], v[114:115]
	v_pk_mul_f32 v[56:57], v[56:57], v[116:117]
	v_cvt_pk_bf16_f32 v54, v54, v55
	v_cvt_pk_bf16_f32 v55, v56, v57
	ds_write_b64 v252, v[54:55]
	v_pk_mul_f32 v[58:59], v[58:59], v[66:67] op_sel_hi:[1,0]
	v_pk_mul_f32 v[60:61], v[60:61], v[66:67] op_sel_hi:[1,0]
	v_pk_mul_f32 v[58:59], v[58:59], v[118:119]
	v_pk_mul_f32 v[60:61], v[60:61], v[120:121]
	v_cvt_pk_bf16_f32 v58, v58, v59
	v_cvt_pk_bf16_f32 v59, v60, v61
	ds_write_b64 v253, v[58:59]
	v_pk_mul_f32 v[62:63], v[62:63], v[66:67] op_sel_hi:[1,0]
	v_pk_mul_f32 v[64:65], v[64:65], v[66:67] op_sel_hi:[1,0]
	v_pk_mul_f32 v[62:63], v[62:63], v[122:123]
	v_pk_mul_f32 v[64:65], v[64:65], v[124:125]
	v_cvt_pk_bf16_f32 v62, v62, v63
	v_cvt_pk_bf16_f32 v63, v64, v65
	ds_write_b64 v254, v[62:63]
	global_load_dwordx4 v[50:53], v[68:69], off offset:352
	global_load_dwordx4 v[54:57], v[68:69], off offset:416
	global_load_dwordx4 v[58:61], v[68:69], off offset:448
	global_load_dwordx4 v[62:65], v[68:69], off offset:480
	v_pk_mul_f32 v[34:35], v[34:35], v[66:67] op_sel_hi:[1,0]
	v_pk_mul_f32 v[36:37], v[36:37], v[66:67] op_sel_hi:[1,0]
	v_pk_mul_f32 v[34:35], v[34:35], v[126:127]
	v_pk_mul_f32 v[36:37], v[36:37], v[128:129]
	v_cvt_pk_bf16_f32 v34, v34, v35
	v_cvt_pk_bf16_f32 v35, v36, v37
	ds_write_b64 v166, v[34:35]
	v_pk_mul_f32 v[38:39], v[38:39], v[66:67] op_sel_hi:[1,0]
	v_pk_mul_f32 v[40:41], v[40:41], v[66:67] op_sel_hi:[1,0]
	v_pk_mul_f32 v[38:39], v[38:39], v[208:209]
	v_pk_mul_f32 v[40:41], v[40:41], v[210:211]
	v_cvt_pk_bf16_f32 v38, v38, v39
	v_cvt_pk_bf16_f32 v39, v40, v41
	ds_write_b64 v191, v[38:39]
	v_pk_mul_f32 v[42:43], v[42:43], v[66:67] op_sel_hi:[1,0]
	v_pk_mul_f32 v[44:45], v[44:45], v[66:67] op_sel_hi:[1,0]
	v_pk_mul_f32 v[42:43], v[42:43], v[212:213]
	v_pk_mul_f32 v[44:45], v[44:45], v[214:215]
	v_cvt_pk_bf16_f32 v42, v42, v43
	v_cvt_pk_bf16_f32 v43, v44, v45
	ds_write_b64 v207, v[42:43]
	v_pk_mul_f32 v[46:47], v[46:47], v[66:67] op_sel_hi:[1,0]
	v_pk_mul_f32 v[48:49], v[48:49], v[66:67] op_sel_hi:[1,0]
	v_pk_mul_f32 v[46:47], v[46:47], v[232:233]
	v_pk_mul_f32 v[48:49], v[48:49], v[234:235]
	v_cvt_pk_bf16_f32 v46, v46, v47
	v_cvt_pk_bf16_f32 v47, v48, v49
	ds_write_b64 v175, v[46:47]
	v_pk_mul_f32 v[18:19], v[18:19], v[66:67] op_sel_hi:[1,0]
	v_pk_mul_f32 v[20:21], v[20:21], v[66:67] op_sel_hi:[1,0]
	v_pk_mul_f32 v[18:19], v[18:19], v[236:237]
	v_pk_mul_f32 v[20:21], v[20:21], v[238:239]
	v_cvt_pk_bf16_f32 v18, v18, v19
	v_cvt_pk_bf16_f32 v19, v20, v21
	ds_write_b64 v177, v[18:19]
	v_pk_mul_f32 v[22:23], v[22:23], v[66:67] op_sel_hi:[1,0]
	v_pk_mul_f32 v[24:25], v[24:25], v[66:67] op_sel_hi:[1,0]
	v_pk_mul_f32 v[22:23], v[22:23], v[240:241]
	v_pk_mul_f32 v[24:25], v[24:25], v[242:243]
	v_cvt_pk_bf16_f32 v22, v22, v23
	v_cvt_pk_bf16_f32 v23, v24, v25
	ds_write_b64 v216, v[22:23]
	v_pk_mul_f32 v[26:27], v[26:27], v[66:67] op_sel_hi:[1,0]
	v_pk_mul_f32 v[28:29], v[28:29], v[66:67] op_sel_hi:[1,0]
	v_pk_mul_f32 v[26:27], v[26:27], v[244:245]
	v_pk_mul_f32 v[28:29], v[28:29], v[246:247]
	v_cvt_pk_bf16_f32 v26, v26, v27
	v_cvt_pk_bf16_f32 v27, v28, v29
	ds_write_b64 v217, v[26:27]
	v_pk_mul_f32 v[2:3], v[2:3], v[66:67] op_sel_hi:[1,0]
	v_pk_mul_f32 v[4:5], v[4:5], v[66:67] op_sel_hi:[1,0]
	v_pk_mul_f32 v[2:3], v[2:3], v[248:249]
	v_pk_mul_f32 v[4:5], v[4:5], v[250:251]
	v_cvt_pk_bf16_f32 v2, v2, v3
	v_cvt_pk_bf16_f32 v3, v4, v5
	ds_write_b64 v219, v[2:3]
	s_waitcnt vmcnt(0)
	v_pk_mul_f32 v[30:31], v[30:31], v[66:67] op_sel_hi:[1,0]
	v_pk_mul_f32 v[32:33], v[32:33], v[66:67] op_sel_hi:[1,0]
	v_pk_mul_f32 v[30:31], v[30:31], v[50:51]
	v_pk_mul_f32 v[32:33], v[32:33], v[52:53]
	v_cvt_pk_bf16_f32 v30, v30, v31
	v_cvt_pk_bf16_f32 v31, v32, v33
	ds_write_b64 v218, v[30:31]
	v_pk_mul_f32 v[6:7], v[6:7], v[66:67] op_sel_hi:[1,0]
	v_pk_mul_f32 v[8:9], v[8:9], v[66:67] op_sel_hi:[1,0]
	v_pk_mul_f32 v[6:7], v[6:7], v[54:55]
	v_pk_mul_f32 v[8:9], v[8:9], v[56:57]
	v_cvt_pk_bf16_f32 v6, v6, v7
	v_cvt_pk_bf16_f32 v7, v8, v9
	ds_write_b64 v220, v[6:7]
	v_pk_mul_f32 v[10:11], v[10:11], v[66:67] op_sel_hi:[1,0]
	v_pk_mul_f32 v[12:13], v[12:13], v[66:67] op_sel_hi:[1,0]
	v_pk_mul_f32 v[10:11], v[10:11], v[58:59]
	v_pk_mul_f32 v[12:13], v[12:13], v[60:61]
	v_cvt_pk_bf16_f32 v10, v10, v11
	v_cvt_pk_bf16_f32 v11, v12, v13
	ds_write_b64 v221, v[10:11]
	v_pk_mul_f32 v[14:15], v[14:15], v[66:67] op_sel_hi:[1,0]
	v_pk_mul_f32 v[16:17], v[16:17], v[66:67] op_sel_hi:[1,0]
	v_pk_mul_f32 v[14:15], v[14:15], v[62:63]
	v_pk_mul_f32 v[16:17], v[16:17], v[64:65]
	v_cvt_pk_bf16_f32 v14, v14, v15
	v_cvt_pk_bf16_f32 v15, v16, v17
	ds_write_b64 v222, v[14:15]
	v_lshlrev_b32_e32 v70, 16, v97
	v_and_b32_e32 v71, 0xffff0000, v97
	v_lshlrev_b32_e32 v72, 16, v90
	v_and_b32_e32 v73, 0xffff0000, v90
	v_lshlrev_b32_e32 v90, 16, v86
	v_and_b32_e32 v91, 0xffff0000, v86
	v_lshlrev_b32_e32 v86, 16, v87
	v_and_b32_e32 v87, 0xffff0000, v87
	v_lshlrev_b32_e32 v92, 16, v88
	v_and_b32_e32 v93, 0xffff0000, v88
	v_lshlrev_b32_e32 v88, 16, v89
	v_and_b32_e32 v89, 0xffff0000, v89
	v_and_b32_e32 v97, 0xffff0000, v83
	v_lshlrev_b64 v[74:75], 11, v[168:169]
	v_lshlrev_b64 v[114:115], 11, v[154:155]
	v_mul_f32_e32 v213, 0xbfb8aa3b, v70
	v_mul_f32_e32 v214, 0xbfb8aa3b, v71
	v_mul_f32_e32 v215, 0xbfb8aa3b, v72
	v_mul_f32_e32 v232, 0xbfb8aa3b, v73
	v_mul_f32_e32 v233, 0xbfb8aa3b, v76
	v_mul_f32_e32 v234, 0xbfb8aa3b, v77
	v_mul_f32_e32 v235, 0xbfb8aa3b, v78
	v_mul_f32_e32 v236, 0xbfb8aa3b, v79
	v_mul_f32_e32 v237, 0xbfb8aa3b, v80
	v_mul_f32_e32 v238, 0xbfb8aa3b, v81
	v_mul_f32_e32 v239, 0xbfb8aa3b, v86
	v_mul_f32_e32 v240, 0xbfb8aa3b, v87
	v_mul_f32_e32 v241, 0xbfb8aa3b, v92
	v_mul_f32_e32 v242, 0xbfb8aa3b, v93
	v_mul_f32_e32 v243, 0xbfb8aa3b, v88
	v_mul_f32_e32 v244, 0xbfb8aa3b, v89
	s_mov_b64 s[0:1], 0
	v_lshlrev_b64 v[60:61], 11, v[170:171]
	v_lshlrev_b32_e32 v58, 16, v94
	v_and_b32_e32 v59, 0xffff0000, v94
	v_lshlrev_b32_e32 v94, 16, v82
	v_lshlrev_b32_e32 v62, 16, v95
	v_and_b32_e32 v63, 0xffff0000, v95
	v_lshlrev_b32_e32 v64, 16, v96
	v_and_b32_e32 v65, 0xffff0000, v96
	v_lshlrev_b32_e32 v96, 16, v83
	v_mul_f32_e32 v209, 0xbfb8aa3b, v62
	v_mul_f32_e32 v210, 0xbfb8aa3b, v63
	v_mul_f32_e32 v211, 0xbfb8aa3b, v64
	v_mul_f32_e32 v212, 0xbfb8aa3b, v65
	v_and_b32_e32 v95, 0xffff0000, v82
	v_lshlrev_b32_e32 v54, 16, v100
	v_and_b32_e32 v55, 0xffff0000, v100
	v_lshlrev_b32_e32 v56, 16, v101
	v_and_b32_e32 v57, 0xffff0000, v101
	v_mul_f32_e32 v169, 0xbfb8aa3b, v54
	v_mul_f32_e32 v170, 0xbfb8aa3b, v55
	v_mul_f32_e32 v171, 0xbfb8aa3b, v56
	v_mul_f32_e32 v208, 0xbfb8aa3b, v57
	v_lshlrev_b32_e32 v100, 16, v84
	v_and_b32_e32 v101, 0xffff0000, v84
	v_lshlrev_b32_e32 v84, 16, v85
	v_and_b32_e32 v85, 0xffff0000, v85
	v_lshlrev_b32_e32 v50, 16, v98
	v_and_b32_e32 v51, 0xffff0000, v98
	v_lshlrev_b32_e32 v52, 16, v99
	v_and_b32_e32 v53, 0xffff0000, v99
	v_lshlrev_b64 v[98:99], 11, v[162:163]
	v_mul_f32_e32 v163, 0xbfb8aa3b, v50
	v_mul_f32_e32 v168, 0xbfb8aa3b, v53
	v_lshlrev_b32_e32 v42, 16, v102
	v_and_b32_e32 v43, 0xffff0000, v102
	v_lshlrev_b32_e32 v44, 16, v103
	v_and_b32_e32 v45, 0xffff0000, v103
	v_lshlrev_b64 v[102:103], 11, v[164:165]
	v_mul_f32_e32 v155, 0xbfb8aa3b, v42
	v_mul_f32_e32 v164, 0xbfb8aa3b, v51
	v_mul_f32_e32 v165, 0xbfb8aa3b, v52
	v_lshlrev_b32_e32 v46, 16, v104
	v_and_b32_e32 v47, 0xffff0000, v104
	v_lshlrev_b32_e32 v48, 16, v105
	v_and_b32_e32 v49, 0xffff0000, v105
	v_lshlrev_b64 v[104:105], 11, v[160:161]
	v_mul_f32_e32 v160, 0xbfb8aa3b, v47
	v_mul_f32_e32 v161, 0xbfb8aa3b, v48
	v_mul_f32_e32 v162, 0xbfb8aa3b, v49
	v_lshlrev_b32_e32 v38, 16, v108
	v_and_b32_e32 v39, 0xffff0000, v108
	v_lshlrev_b32_e32 v40, 16, v109
	v_and_b32_e32 v41, 0xffff0000, v109
	v_mul_f32_e32 v127, 0xbfb8aa3b, v38
	v_mul_f32_e32 v128, 0xbfb8aa3b, v39
	v_mul_f32_e32 v129, 0xbfb8aa3b, v40
	v_mul_f32_e32 v154, 0xbfb8aa3b, v41
	v_lshlrev_b32_e32 v34, 16, v106
	v_and_b32_e32 v35, 0xffff0000, v106
	v_lshlrev_b32_e32 v36, 16, v107
	v_and_b32_e32 v37, 0xffff0000, v107
	v_mul_f32_e32 v123, 0xbfb8aa3b, v34
	v_mul_f32_e32 v124, 0xbfb8aa3b, v35
	v_mul_f32_e32 v125, 0xbfb8aa3b, v36
	v_mul_f32_e32 v126, 0xbfb8aa3b, v37
	v_lshlrev_b32_e32 v26, 16, v112
	v_and_b32_e32 v27, 0xffff0000, v112
	v_lshlrev_b32_e32 v28, 16, v113
	v_and_b32_e32 v29, 0xffff0000, v113
	v_lshlrev_b64 v[112:113], 11, v[156:157]
	v_mul_f32_e32 v119, 0xbfb8aa3b, v26
	v_mul_f32_e32 v120, 0xbfb8aa3b, v27
	v_mul_f32_e32 v121, 0xbfb8aa3b, v28
	v_mul_f32_e32 v122, 0xbfb8aa3b, v29
	v_mul_f32_e32 v156, 0xbfb8aa3b, v43
	v_mul_f32_e32 v157, 0xbfb8aa3b, v44
	v_lshl_add_u64 v[82:83], v[144:145], 0, v[112:113]
	v_mul_f32_e32 v112, 0xbfb8aa3b, v94
	v_mul_f32_e32 v113, 0xbfb8aa3b, v95
	v_exp_f32_e32 v112, v112
	v_exp_f32_e32 v113, v113
	v_add_f32_e32 v247, 1.0, v112
	v_add_f32_e32 v248, 1.0, v113
	v_lshlrev_b32_e32 v22, 16, v110
	v_mul_f32_e32 v67, 0xbfb8aa3b, v22
	v_exp_f32_e32 v67, v67
	v_and_b32_e32 v23, 0xffff0000, v110
	v_lshlrev_b32_e32 v24, 16, v111
	v_and_b32_e32 v25, 0xffff0000, v111
	v_lshlrev_b64 v[110:111], 11, v[158:159]
	v_mul_f32_e32 v116, 0xbfb8aa3b, v23
	v_mul_f32_e32 v117, 0xbfb8aa3b, v24
	v_mul_f32_e32 v118, 0xbfb8aa3b, v25
	v_mul_f32_e32 v158, 0xbfb8aa3b, v45
	v_mul_f32_e32 v159, 0xbfb8aa3b, v46
	v_add_f32_e32 v67, 1.0, v67
	v_lshl_add_u64 v[18:19], v[144:145], 0, v[60:61]
	v_lshl_add_u64 v[30:31], v[144:145], 0, v[102:103]
	v_lshl_add_u64 v[60:61], v[144:145], 0, v[104:105]
	v_lshl_add_u64 v[20:21], v[144:145], 0, v[74:75]
	v_lshl_add_u64 v[32:33], v[144:145], 0, v[98:99]
	v_mul_f32_e32 v98, 0xbfb8aa3b, v58
	v_mul_f32_e32 v99, 0xbfb8aa3b, v59
	v_lshl_add_u64 v[74:75], v[144:145], 0, v[110:111]
	v_mul_f32_e32 v110, 0xbfb8aa3b, v90
	v_mul_f32_e32 v111, 0xbfb8aa3b, v91
	v_exp_f32_e32 v98, v98
	v_exp_f32_e32 v99, v99
	v_exp_f32_e32 v110, v110
	v_exp_f32_e32 v111, v111
	v_add_f32_e32 v245, 1.0, v110
	v_add_f32_e32 v246, 1.0, v111
	v_mul_f32_e32 v4, 0xbfb8aa3b, v96
	v_mul_f32_e32 v5, 0xbfb8aa3b, v97
	v_lshl_add_u64 v[2:3], v[144:145], 0, v[114:115]
	v_exp_f32_e32 v114, v116
	v_exp_f32_e32 v115, v117
	v_exp_f32_e32 v116, v118
	v_exp_f32_e32 v117, v119
	v_exp_f32_e32 v118, v120
	v_exp_f32_e32 v119, v121
	v_exp_f32_e32 v120, v122
	v_exp_f32_e32 v121, v123
	v_exp_f32_e32 v122, v124
	v_exp_f32_e32 v123, v125
	v_exp_f32_e32 v124, v126
	v_exp_f32_e32 v125, v127
	v_exp_f32_e32 v126, v128
	v_exp_f32_e32 v127, v129
	v_exp_f32_e32 v128, v154
	v_exp_f32_e32 v129, v155
	v_exp_f32_e32 v154, v156
	v_exp_f32_e32 v155, v157
	v_exp_f32_e32 v156, v158
	v_exp_f32_e32 v157, v159
	v_exp_f32_e32 v158, v160
	v_exp_f32_e32 v159, v161
	v_exp_f32_e32 v160, v162
	v_exp_f32_e32 v161, v163
	v_exp_f32_e32 v162, v164
	v_exp_f32_e32 v163, v165
	v_exp_f32_e32 v164, v168
	v_exp_f32_e32 v165, v169
	v_exp_f32_e32 v168, v170
	v_exp_f32_e32 v169, v171
	v_exp_f32_e32 v170, v208
	v_exp_f32_e32 v171, v209
	v_exp_f32_e32 v208, v210
	v_exp_f32_e32 v209, v211
	v_exp_f32_e32 v210, v212
	v_exp_f32_e32 v211, v213
	v_exp_f32_e32 v212, v214
	v_exp_f32_e32 v213, v215
	v_exp_f32_e32 v214, v232
	v_exp_f32_e32 v215, v233
	v_exp_f32_e32 v232, v234
	v_exp_f32_e32 v233, v235
	v_exp_f32_e32 v234, v236
	v_exp_f32_e32 v235, v237
	v_exp_f32_e32 v236, v238
	v_exp_f32_e32 v237, v239
	v_exp_f32_e32 v238, v240
	v_exp_f32_e32 v239, v241
	v_exp_f32_e32 v240, v242
	v_exp_f32_e32 v241, v243
	v_exp_f32_e32 v242, v244
	v_exp_f32_e32 v243, v4
	v_exp_f32_e32 v244, v5
	v_mul_f32_e32 v106, 0xbfb8aa3b, v100
	v_add_f32_e32 v114, 1.0, v114
	v_mul_f32_e32 v107, 0xbfb8aa3b, v101
	v_mul_f32_e32 v108, 0xbfb8aa3b, v84
	v_mul_f32_e32 v109, 0xbfb8aa3b, v85
	v_exp_f32_e32 v106, v106
	v_rcp_f32_e32 v8, v67
	v_rcp_f32_e32 v9, v114
	v_exp_f32_e32 v107, v107
	v_exp_f32_e32 v108, v108
	v_exp_f32_e32 v109, v109
	v_add_f32_e32 v118, 1.0, v118
	v_add_f32_e32 v234, 1.0, v234
	v_add_f32_e32 v235, 1.0, v235
	v_add_f32_e32 v115, 1.0, v115
	v_add_f32_e32 v116, 1.0, v116
	v_add_f32_e32 v117, 1.0, v117
	v_add_f32_e32 v249, 1.0, v106
	v_add_f32_e32 v250, 1.0, v107
	v_add_f32_e32 v251, 1.0, v108
	v_add_f32_e32 v179, 1.0, v109
	v_add_f32_e32 v104, 1.0, v119
	v_add_f32_e32 v105, 1.0, v120
	v_add_f32_e32 v119, 1.0, v121
	v_add_f32_e32 v120, 1.0, v122
	v_add_f32_e32 v121, 1.0, v123
	v_add_f32_e32 v122, 1.0, v124
	v_add_f32_e32 v123, 1.0, v125
	v_add_f32_e32 v124, 1.0, v126
	v_add_f32_e32 v125, 1.0, v127
	v_add_f32_e32 v126, 1.0, v128
	v_add_f32_e32 v127, 1.0, v129
	v_add_f32_e32 v128, 1.0, v154
	v_add_f32_e32 v129, 1.0, v155
	v_add_f32_e32 v154, 1.0, v156
	v_add_f32_e32 v155, 1.0, v157
	v_add_f32_e32 v156, 1.0, v158
	v_add_f32_e32 v157, 1.0, v159
	v_add_f32_e32 v158, 1.0, v160
	v_add_f32_e32 v159, 1.0, v161
	v_add_f32_e32 v160, 1.0, v162
	v_add_f32_e32 v161, 1.0, v163
	v_add_f32_e32 v162, 1.0, v164
	v_rcp_f32_e32 v103, v118
	v_rcp_f32_e32 v106, v119
	v_rcp_f32_e32 v118, v161
	v_rcp_f32_e32 v119, v162
	v_rcp_f32_e32 v161, v234
	v_rcp_f32_e32 v162, v235
	v_pk_mul_f32 v[234:235], v[8:9], v[22:23]
	v_add_f32_e32 v163, 1.0, v165
	v_add_f32_e32 v164, 1.0, v168
	v_add_f32_e32 v165, 1.0, v169
	v_add_f32_e32 v168, 1.0, v170
	v_add_f32_e32 v169, 1.0, v98
	v_add_f32_e32 v170, 1.0, v99
	v_rcp_f32_e32 v98, v115
	v_rcp_f32_e32 v99, v116
	v_rcp_f32_e32 v102, v117
	v_rcp_f32_e32 v104, v104
	v_rcp_f32_e32 v105, v105
	v_rcp_f32_e32 v107, v120
	v_rcp_f32_e32 v108, v121
	v_rcp_f32_e32 v109, v122
	v_rcp_f32_e32 v110, v123
	v_rcp_f32_e32 v111, v124
	v_rcp_f32_e32 v112, v125
	v_rcp_f32_e32 v113, v126
	v_rcp_f32_e32 v114, v127
	v_rcp_f32_e32 v115, v128
	v_rcp_f32_e32 v116, v129
	v_rcp_f32_e32 v117, v154
	v_add_f32_e32 v171, 1.0, v171
	v_add_f32_e32 v208, 1.0, v208
	v_add_f32_e32 v209, 1.0, v209
	v_add_f32_e32 v210, 1.0, v210
	v_add_f32_e32 v211, 1.0, v211
	v_add_f32_e32 v212, 1.0, v212
	v_add_f32_e32 v213, 1.0, v213
	v_add_f32_e32 v214, 1.0, v214
	v_add_f32_e32 v215, 1.0, v215
	v_add_f32_e32 v232, 1.0, v232
	v_add_f32_e32 v233, 1.0, v233
	v_add_f32_e32 v236, 1.0, v236
	v_add_f32_e32 v237, 1.0, v237
	v_add_f32_e32 v238, 1.0, v238
	v_add_f32_e32 v239, 1.0, v239
	v_add_f32_e32 v240, 1.0, v240
	v_add_f32_e32 v241, 1.0, v241
	v_add_f32_e32 v242, 1.0, v242
	v_add_f32_e32 v243, 1.0, v243
	v_add_f32_e32 v244, 1.0, v244
	v_pk_mul_f32 v[98:99], v[98:99], v[24:25]
	v_pk_mul_f32 v[102:103], v[102:103], v[26:27]
	v_pk_mul_f32 v[104:105], v[104:105], v[28:29]
	v_pk_mul_f32 v[106:107], v[106:107], v[34:35]
	v_pk_mul_f32 v[108:109], v[108:109], v[36:37]
	v_pk_mul_f32 v[110:111], v[110:111], v[38:39]
	v_pk_mul_f32 v[112:113], v[112:113], v[40:41]
	v_rcp_f32_e32 v10, v155
	v_rcp_f32_e32 v11, v156
	v_rcp_f32_e32 v12, v157
	v_rcp_f32_e32 v13, v158
	v_pk_mul_f32 v[114:115], v[114:115], v[42:43]
	v_pk_mul_f32 v[46:47], v[10:11], v[46:47]
	v_pk_mul_f32 v[116:117], v[116:117], v[44:45]
	v_pk_mul_f32 v[48:49], v[12:13], v[48:49]
	v_rcp_f32_e32 v68, v159
	v_rcp_f32_e32 v69, v160
	v_rcp_f32_e32 v120, v163
	v_rcp_f32_e32 v121, v164
	v_rcp_f32_e32 v122, v165
	v_rcp_f32_e32 v123, v168
	v_rcp_f32_e32 v124, v169
	v_rcp_f32_e32 v125, v170
	v_rcp_f32_e32 v126, v171
	v_rcp_f32_e32 v127, v208
	v_rcp_f32_e32 v128, v209
	v_rcp_f32_e32 v129, v210
	v_rcp_f32_e32 v154, v211
	v_rcp_f32_e32 v155, v212
	v_rcp_f32_e32 v156, v213
	v_rcp_f32_e32 v157, v214
	v_rcp_f32_e32 v158, v215
	v_rcp_f32_e32 v159, v232
	v_rcp_f32_e32 v160, v233
	v_rcp_f32_e32 v163, v236
	v_rcp_f32_e32 v164, v245
	v_rcp_f32_e32 v165, v246
	v_rcp_f32_e32 v168, v237
	v_rcp_f32_e32 v169, v238
	v_rcp_f32_e32 v170, v239
	v_rcp_f32_e32 v171, v240
	v_rcp_f32_e32 v208, v241
	v_rcp_f32_e32 v209, v242
	v_rcp_f32_e32 v210, v247
	v_rcp_f32_e32 v211, v248
	v_rcp_f32_e32 v212, v243
	v_rcp_f32_e32 v213, v244
	v_rcp_f32_e32 v214, v249
	v_rcp_f32_e32 v215, v250
	v_rcp_f32_e32 v232, v251
	v_rcp_f32_e32 v233, v179
	v_pk_mul_f32 v[50:51], v[68:69], v[50:51]
	v_pk_mul_f32 v[52:53], v[118:119], v[52:53]
	v_pk_mul_f32 v[54:55], v[120:121], v[54:55]
	v_pk_mul_f32 v[56:57], v[122:123], v[56:57]
	v_pk_mul_f32 v[58:59], v[124:125], v[58:59]
	v_pk_mul_f32 v[62:63], v[126:127], v[62:63]
	v_pk_mul_f32 v[64:65], v[128:129], v[64:65]
	v_pk_mul_f32 v[68:69], v[154:155], v[70:71]
	v_pk_mul_f32 v[70:71], v[156:157], v[72:73]
	v_pk_mul_f32 v[72:73], v[158:159], v[76:77]
	v_pk_mul_f32 v[76:77], v[160:161], v[78:79]
	v_pk_mul_f32 v[78:79], v[162:163], v[80:81]
	v_pk_mul_f32 v[80:81], v[164:165], v[90:91]
	v_pk_mul_f32 v[86:87], v[168:169], v[86:87]
	v_pk_mul_f32 v[90:91], v[170:171], v[92:93]
	v_pk_mul_f32 v[88:89], v[208:209], v[88:89]
	v_pk_mul_f32 v[92:93], v[210:211], v[94:95]
	v_pk_mul_f32 v[94:95], v[212:213], v[96:97]
	v_pk_mul_f32 v[96:97], v[214:215], v[100:101]
	v_pk_mul_f32 v[84:85], v[232:233], v[84:85]
	s_waitcnt lgkmcnt(0)
	s_barrier
	ds_read_b128 v[4:7], v223
	ds_read_b128 v[8:11], v224
	ds_read_b128 v[12:15], v225
	ds_read_b128 v[22:25], v226
	ds_read_b128 v[26:29], v227
	ds_read_b128 v[34:37], v228
	ds_read_b128 v[38:41], v229
	ds_read_b128 v[42:45], v230
	s_waitcnt lgkmcnt(7)
	v_lshlrev_b32_e32 v16, 16, v4
	v_and_b32_e32 v17, 0xffff0000, v4
	v_lshlrev_b32_e32 v4, 16, v5
	v_and_b32_e32 v5, 0xffff0000, v5
	v_lshlrev_b32_e32 v66, 16, v6
	v_and_b32_e32 v67, 0xffff0000, v6
	v_lshlrev_b32_e32 v6, 16, v7
	v_and_b32_e32 v7, 0xffff0000, v7
	s_waitcnt lgkmcnt(6)
	v_lshlrev_b32_e32 v100, 16, v8
	v_and_b32_e32 v101, 0xffff0000, v8
	v_lshlrev_b32_e32 v8, 16, v9
	v_and_b32_e32 v9, 0xffff0000, v9
	v_lshlrev_b32_e32 v118, 16, v10
	v_and_b32_e32 v119, 0xffff0000, v10
	v_lshlrev_b32_e32 v10, 16, v11
	v_and_b32_e32 v11, 0xffff0000, v11
	s_waitcnt lgkmcnt(5)
	v_lshlrev_b32_e32 v120, 16, v12
	v_and_b32_e32 v121, 0xffff0000, v12
	v_lshlrev_b32_e32 v12, 16, v13
	v_and_b32_e32 v13, 0xffff0000, v13
	v_lshlrev_b32_e32 v122, 16, v14
	v_and_b32_e32 v123, 0xffff0000, v14
	v_lshlrev_b32_e32 v14, 16, v15
	v_and_b32_e32 v15, 0xffff0000, v15
	s_waitcnt lgkmcnt(4)
	v_lshlrev_b32_e32 v124, 16, v22
	v_and_b32_e32 v125, 0xffff0000, v22
	v_lshlrev_b32_e32 v22, 16, v23
	v_and_b32_e32 v23, 0xffff0000, v23
	v_lshlrev_b32_e32 v126, 16, v24
	v_and_b32_e32 v127, 0xffff0000, v24
	v_lshlrev_b32_e32 v24, 16, v25
	v_and_b32_e32 v25, 0xffff0000, v25
	s_waitcnt lgkmcnt(3)
	v_lshlrev_b32_e32 v128, 16, v26
	v_and_b32_e32 v129, 0xffff0000, v26
	v_lshlrev_b32_e32 v26, 16, v27
	v_and_b32_e32 v27, 0xffff0000, v27
	v_lshlrev_b32_e32 v154, 16, v28
	v_and_b32_e32 v155, 0xffff0000, v28
	v_lshlrev_b32_e32 v28, 16, v29
	v_and_b32_e32 v29, 0xffff0000, v29
	s_waitcnt lgkmcnt(2)
	v_lshlrev_b32_e32 v156, 16, v34
	v_and_b32_e32 v157, 0xffff0000, v34
	v_lshlrev_b32_e32 v34, 16, v35
	v_and_b32_e32 v35, 0xffff0000, v35
	v_lshlrev_b32_e32 v158, 16, v36
	v_and_b32_e32 v159, 0xffff0000, v36
	v_lshlrev_b32_e32 v36, 16, v37
	v_and_b32_e32 v37, 0xffff0000, v37
	s_waitcnt lgkmcnt(1)
	v_lshlrev_b32_e32 v160, 16, v38
	v_and_b32_e32 v161, 0xffff0000, v38
	v_lshlrev_b32_e32 v38, 16, v39
	v_and_b32_e32 v39, 0xffff0000, v39
	v_lshlrev_b32_e32 v162, 16, v40
	v_and_b32_e32 v163, 0xffff0000, v40
	v_lshlrev_b32_e32 v40, 16, v41
	v_and_b32_e32 v41, 0xffff0000, v41
	s_waitcnt lgkmcnt(0)
	v_lshlrev_b32_e32 v164, 16, v42
	v_and_b32_e32 v165, 0xffff0000, v42
	v_lshlrev_b32_e32 v42, 16, v43
	v_and_b32_e32 v43, 0xffff0000, v43
	v_lshlrev_b32_e32 v168, 16, v44
	v_and_b32_e32 v169, 0xffff0000, v44
	v_lshlrev_b32_e32 v44, 16, v45
	v_and_b32_e32 v45, 0xffff0000, v45
	v_pk_mul_f32 v[16:17], v[234:235], v[16:17]
	v_pk_mul_f32 v[98:99], v[98:99], v[4:5]
	v_pk_mul_f32 v[66:67], v[102:103], v[66:67]
	v_pk_mul_f32 v[102:103], v[104:105], v[6:7]
	v_pk_mul_f32 v[100:101], v[106:107], v[100:101]
	v_pk_mul_f32 v[104:105], v[108:109], v[8:9]
	v_pk_mul_f32 v[106:107], v[110:111], v[118:119]
	v_pk_mul_f32 v[108:109], v[112:113], v[10:11]
	v_pk_mul_f32 v[110:111], v[114:115], v[120:121]
	v_pk_mul_f32 v[112:113], v[116:117], v[12:13]
	v_pk_mul_f32 v[46:47], v[46:47], v[122:123]
	v_pk_mul_f32 v[48:49], v[48:49], v[14:15]
	v_pk_mul_f32 v[50:51], v[50:51], v[124:125]
	v_pk_mul_f32 v[52:53], v[52:53], v[22:23]
	v_pk_mul_f32 v[54:55], v[54:55], v[126:127]
	v_pk_mul_f32 v[56:57], v[56:57], v[24:25]
	v_pk_mul_f32 v[58:59], v[58:59], v[128:129]
	v_pk_mul_f32 v[62:63], v[62:63], v[26:27]
	v_pk_mul_f32 v[64:65], v[64:65], v[154:155]
	v_pk_mul_f32 v[68:69], v[68:69], v[28:29]
	v_pk_mul_f32 v[70:71], v[70:71], v[156:157]
	v_pk_mul_f32 v[72:73], v[72:73], v[34:35]
	v_pk_mul_f32 v[76:77], v[76:77], v[158:159]
	v_pk_mul_f32 v[78:79], v[78:79], v[36:37]
	v_pk_mul_f32 v[80:81], v[80:81], v[160:161]
	v_pk_mul_f32 v[86:87], v[86:87], v[38:39]
	v_pk_mul_f32 v[90:91], v[90:91], v[162:163]
	v_pk_mul_f32 v[88:89], v[88:89], v[40:41]
	v_pk_mul_f32 v[92:93], v[92:93], v[164:165]
	v_pk_mul_f32 v[94:95], v[94:95], v[42:43]
	v_pk_mul_f32 v[96:97], v[96:97], v[168:169]
	v_pk_mul_f32 v[84:85], v[84:85], v[44:45]
	v_cvt_pk_bf16_f32 v4, v16, v17
	v_cvt_pk_bf16_f32 v5, v98, v99
	v_cvt_pk_bf16_f32 v6, v66, v67
	v_cvt_pk_bf16_f32 v7, v102, v103
	v_cvt_pk_bf16_f32 v8, v100, v101
	v_cvt_pk_bf16_f32 v9, v104, v105
	v_cvt_pk_bf16_f32 v10, v106, v107
	v_cvt_pk_bf16_f32 v11, v108, v109
	v_cvt_pk_bf16_f32 v12, v110, v111
	v_cvt_pk_bf16_f32 v13, v112, v113
	v_cvt_pk_bf16_f32 v14, v46, v47
	v_cvt_pk_bf16_f32 v15, v48, v49
	v_cvt_pk_bf16_f32 v22, v50, v51
	v_cvt_pk_bf16_f32 v23, v52, v53
	v_cvt_pk_bf16_f32 v24, v54, v55
	v_cvt_pk_bf16_f32 v25, v56, v57
	v_cvt_pk_bf16_f32 v26, v58, v59
	v_cvt_pk_bf16_f32 v27, v62, v63
	v_cvt_pk_bf16_f32 v28, v64, v65
	v_cvt_pk_bf16_f32 v29, v68, v69
	v_cvt_pk_bf16_f32 v34, v70, v71
	v_cvt_pk_bf16_f32 v35, v72, v73
	v_cvt_pk_bf16_f32 v36, v76, v77
	v_cvt_pk_bf16_f32 v37, v78, v79
	v_cvt_pk_bf16_f32 v38, v80, v81
	v_cvt_pk_bf16_f32 v39, v86, v87
	v_cvt_pk_bf16_f32 v40, v90, v91
	v_cvt_pk_bf16_f32 v41, v88, v89
	v_cvt_pk_bf16_f32 v42, v92, v93
	v_cvt_pk_bf16_f32 v43, v94, v95
	v_cvt_pk_bf16_f32 v44, v96, v97
	v_cvt_pk_bf16_f32 v45, v84, v85
	global_store_dwordx4 v[18:19], v[4:7], off
	global_store_dwordx4 v[20:21], v[8:11], off
	global_store_dwordx4 v[30:31], v[12:15], off
	global_store_dwordx4 v[32:33], v[22:25], off
	global_store_dwordx4 v[60:61], v[26:29], off
	global_store_dwordx4 v[74:75], v[34:37], off
	global_store_dwordx4 v[82:83], v[38:41], off
	global_store_dwordx4 v[2:3], v[42:45], off
	s_waitcnt lgkmcnt(0)
	s_barrier

.LBB0_1417:
	s_or_b64 exec, exec, s[0:1]
	s_waitcnt lgkmcnt(0)
	s_barrier
	v_mov_b32_e32 v2, s80
	ds_read_b32 v2, v2
	s_waitcnt lgkmcnt(0)
	s_barrier
	s_movk_i32 s0, 0xff
	s_waitcnt lgkmcnt(0)
	v_cmp_lt_i32_e32 vcc, s0, v2
	v_readfirstlane_b32 s74, v2
	s_mov_b64 s[0:1], -1
	s_cbranch_vccnz .LBB0_1412
	v_mov_b32_e32 v2, s81
	v_mov_b32_e32 v3, s82
	ds_read_b32 v2, v2
	ds_read_b32 v3, v3
	v_or_b32_e32 v18, 32, v167
	v_mov_b32_e32 v91, v192
	v_or_b32_e32 v92, 0xfffffe00, v0
	s_waitcnt lgkmcnt(1)
	v_readfirstlane_b32 s0, v2
	s_waitcnt lgkmcnt(0)
	v_readfirstlane_b32 s1, v3
	s_nop 1
	v_lshl_add_u64 v[2:3], v[132:133], 2, s[0:1]
	v_add_co_u32_e32 v12, vcc, s83, v2
	v_lshl_add_u64 v[4:5], v[146:147], 2, s[0:1]
	v_lshl_add_u64 v[6:7], v[136:137], 2, s[0:1]
	v_lshl_add_u64 v[8:9], v[138:139], 2, s[0:1]
	v_lshl_add_u64 v[10:11], v[140:141], 2, s[0:1]
	v_addc_co_u32_e32 v13, vcc, 0, v3, vcc
	global_load_dword v22, v[2:3], off
	global_load_dword v23, v[4:5], off offset:1024
	global_load_dword v20, v[4:5], off offset:2048
	global_load_dword v21, v[4:5], off offset:3072
	global_load_dword v24, v[6:7], off
	global_load_dword v25, v[8:9], off
	global_load_dword v88, v[10:11], off
	global_load_dword v89, v[12:13], off offset:3072
	v_mov_b32_e32 v2, s84
	v_mov_b32_e32 v3, s85
	ds_read_b32 v2, v2
	ds_read_b32 v3, v3
	s_lshl_b32 s0, s74, 6
	v_or_b32_e32 v160, s0, v18
	v_or_b32_e32 v18, 48, v167
	s_waitcnt lgkmcnt(0)
	v_readfirstlane_b32 s1, v2
	v_readfirstlane_b32 s33, v3
	v_or_b32_e32 v156, s0, v18
	v_lshrrev_b32_e32 v18, 5, v0
	v_mov_b32_e32 v2, s1
	v_mov_b32_e32 v3, s33
	v_or_b32_e32 v170, s0, v167
	v_or_b32_e32 v164, s0, v173
	v_or_b32_e32 v18, s0, v18
	v_lshl_add_u64 v[2:3], v[130:131], 2, v[2:3]
	v_mad_i64_i32 v[74:75], s[76:77], v170, s92, v[148:149]
	v_or_b32_e32 v168, s0, v172
	v_mad_i64_i32 v[78:79], s[76:77], v164, s92, v[148:149]
	v_or_b32_e32 v162, s0, v174
	v_mad_i64_i32 v[82:83], s[76:77], v160, s92, v[148:149]
	v_or_b32_e32 v158, s0, v176
	v_mad_i64_i32 v[86:87], s[76:77], v156, s92, v[148:149]
	v_or_b32_e32 v154, s0, v178
	v_mad_i64_i32 v[18:19], s[76:77], v18, s92, v[150:151]
	global_load_dword v90, v[2:3], off
	v_mad_i64_i32 v[76:77], s[76:77], v168, s92, v[148:149]
	global_load_dwordx4 v[2:5], v[74:75], off offset:1024
	global_load_dwordx4 v[6:9], v[76:77], off offset:1024
	v_mad_i64_i32 v[80:81], s[76:77], v162, s92, v[148:149]
	global_load_dwordx4 v[10:13], v[78:79], off offset:1024
	global_load_dwordx4 v[14:17], v[80:81], off offset:1024
	v_mad_i64_i32 v[84:85], s[76:77], v158, s92, v[148:149]
	global_load_dwordx4 v[26:29], v[82:83], off offset:1024
	global_load_dwordx4 v[30:33], v[84:85], off offset:1024
	v_mad_i64_i32 v[114:115], s[76:77], v154, s92, v[148:149]
	global_load_dwordx4 v[34:37], v[86:87], off offset:1024
	global_load_dwordx4 v[38:41], v[114:115], off offset:1024
	global_load_dwordx4 v[42:45], v[18:19], off
	global_load_dwordx4 v[46:49], v[18:19], off offset:512
	v_or_b32_e32 v18, s0, v180
	v_mad_i64_i32 v[18:19], s[76:77], v18, s92, v[150:151]
	global_load_dwordx4 v[50:53], v[18:19], off
	global_load_dwordx4 v[54:57], v[18:19], off offset:512
	v_or_b32_e32 v18, s0, v181
	v_mad_i64_i32 v[18:19], s[76:77], v18, s92, v[150:151]
	global_load_dwordx4 v[58:61], v[18:19], off
	global_load_dwordx4 v[62:65], v[18:19], off offset:512
	v_or_b32_e32 v18, s0, v182
	v_mad_i64_i32 v[18:19], s[76:77], v18, s92, v[150:151]
	global_load_dwordx4 v[66:69], v[18:19], off
	global_load_dwordx4 v[70:73], v[18:19], off offset:512
	s_ashr_i32 s1, s0, 31
	s_lshl_b64 s[0:1], s[0:1], 6
	v_ashrrev_i32_e32 v171, 31, v170
	v_ashrrev_i32_e32 v169, 31, v168
	v_ashrrev_i32_e32 v165, 31, v164
	v_ashrrev_i32_e32 v163, 31, v162
	v_ashrrev_i32_e32 v161, 31, v160
	v_ashrrev_i32_e32 v159, 31, v158
	v_ashrrev_i32_e32 v157, 31, v156
	v_ashrrev_i32_e32 v155, 31, v154
	v_lshl_add_u64 v[18:19], v[152:153], 0, s[0:1]
	s_mov_b64 s[0:1], 0
	global_load_dword v93, v[18:19], off
	global_load_dword v92, v[18:19], off offset:2048
	s_waitcnt vmcnt(0)
	ds_write_b32 v91, v93
	ds_write_b32 v91, v92 offset:2048
	s_or_b64 exec, exec, s[0:1]
	ds_write_b128 v183, v[42:45] offset:6144
	ds_write_b128 v183, v[46:49] offset:43008
	ds_write_b128 v184, v[50:53] offset:6144
	ds_write_b128 v184, v[54:57] offset:43008
	ds_write_b128 v185, v[58:61] offset:6144
	ds_write_b128 v185, v[62:65] offset:43008
	ds_write_b128 v186, v[66:69] offset:6144
	ds_write_b128 v186, v[70:73] offset:43008
	ds_write_b128 v223, v[2:5]
	ds_write_b128 v224, v[6:9]
	ds_write_b128 v225, v[10:13]
	ds_write_b128 v226, v[14:17]
	ds_write_b128 v227, v[26:29]
	ds_write_b128 v228, v[30:33]
	ds_write_b128 v229, v[34:37]
	ds_write_b128 v230, v[38:41]
	s_waitcnt lgkmcnt(0)
	s_barrier
	v_cvt_pk_bf16_f32 v18, v22, v23
	ds_read_b128 v[26:29], v187
	ds_read_b128 v[30:33], v187 offset:16
	v_lshlrev_b32_e32 v92, 16, v18
	v_and_b32_e32 v93, 0xffff0000, v18
	v_cvt_pk_bf16_f32 v19, v20, v21
	v_pk_add_f32 v[22:23], v[22:23], v[92:93] neg_lo:[0,1] neg_hi:[0,1]
	v_lshlrev_b32_e32 v92, 16, v19
	v_and_b32_e32 v93, 0xffff0000, v19
	v_pk_add_f32 v[20:21], v[20:21], v[92:93] neg_lo:[0,1] neg_hi:[0,1]
	v_cvt_pk_bf16_f32 v22, v22, v23
	v_cvt_pk_bf16_f32 v23, v20, v21
	v_cvt_pk_bf16_f32 v20, v24, v25
	v_lshlrev_b32_e32 v92, 16, v20
	v_and_b32_e32 v93, 0xffff0000, v20
	v_cvt_pk_bf16_f32 v21, v88, v89
	s_waitcnt lgkmcnt(0)
	v_cvt_pk_bf16_f32 v34, v26, v27
	v_cvt_pk_bf16_f32 v35, v28, v29
	v_cvt_pk_bf16_f32 v36, v30, v31
	v_cvt_pk_bf16_f32 v37, v32, v33
	v_pk_add_f32 v[24:25], v[24:25], v[92:93] neg_lo:[0,1] neg_hi:[0,1]
	v_lshlrev_b32_e32 v92, 16, v21
	v_and_b32_e32 v93, 0xffff0000, v21
	v_pk_add_f32 v[2:3], v[88:89], v[92:93] neg_lo:[0,1] neg_hi:[0,1]
	v_cvt_pk_bf16_f32 v24, v24, v25
	v_cvt_pk_bf16_f32 v25, v2, v3
	v_lshlrev_b32_e32 v2, 16, v34
	v_and_b32_e32 v3, 0xffff0000, v34
	v_pk_add_f32 v[2:3], v[26:27], v[2:3] neg_lo:[0,1] neg_hi:[0,1]
	v_lshlrev_b32_e32 v38, 16, v35
	v_cvt_pk_bf16_f32 v26, v2, v3
	v_mfma_f32_32x32x16_bf16 v[2:17], v[34:37], v[18:21], 0
	v_and_b32_e32 v39, 0xffff0000, v35
	v_add_f32_e64 v28, v28, -v38
	v_add_f32_e64 v29, v29, -v39
	ds_read_b128 v[44:47], v187 offset:2048
	ds_read_b128 v[48:51], v187 offset:2064
	v_cvt_pk_bf16_f32 v27, v28, v29
	v_lshlrev_b32_e32 v28, 16, v36
	v_and_b32_e32 v29, 0xffff0000, v36
	v_mfma_f32_32x32x16_bf16 v[2:17], v[34:37], v[22:25], v[2:17]
	v_add_f32_e64 v28, v30, -v28
	v_add_f32_e64 v29, v31, -v29
	v_lshlrev_b32_e32 v30, 16, v37
	v_and_b32_e32 v31, 0xffff0000, v37
	v_add_f32_e64 v30, v32, -v30
	v_add_f32_e64 v31, v33, -v31
	v_cvt_pk_bf16_f32 v28, v28, v29
	v_cvt_pk_bf16_f32 v29, v30, v31
	s_waitcnt lgkmcnt(1)
	v_cvt_pk_bf16_f32 v52, v44, v45
	v_cvt_pk_bf16_f32 v53, v46, v47
	v_mfma_f32_32x32x16_bf16 v[2:17], v[26:29], v[18:21], v[2:17]
	s_waitcnt lgkmcnt(0)
	v_cvt_pk_bf16_f32 v54, v48, v49
	v_cvt_pk_bf16_f32 v55, v50, v51
	v_lshlrev_b32_e32 v56, 16, v53
	v_and_b32_e32 v57, 0xffff0000, v53
	v_pk_add_f32 v[46:47], v[46:47], v[56:57] neg_lo:[0,1] neg_hi:[0,1]
	s_nop 5
	v_add_f32_e32 v2, v90, v2
	v_mul_f32_e64 v26, |v2|, s93
	v_exp_f32_e32 v26, v26
	v_add_f32_e32 v3, v90, v3
	v_mul_f32_e64 v28, |v3|, s93
	v_exp_f32_e32 v28, v28
	v_add_f32_e32 v26, 1.0, v26
	v_add_f32_e32 v4, v90, v4
	v_add_f32_e32 v28, 1.0, v28
	v_log_f32_e32 v26, v26
	v_min_f32_e32 v2, 0, v2
	v_add_f32_e32 v5, v90, v5
	v_add_f32_e32 v7, v90, v7
	v_mul_f32_e32 v27, 0x3f317217, v26
	v_fma_f32 v27, v26, s95, -v27
	v_fmac_f32_e32 v27, 0x3377d1cf, v26
	v_fmac_f32_e32 v27, 0x3f317217, v26
	s_nop 1
	v_mov_b32_e32 v26, v27
	v_mul_f32_e64 v27, |v4|, s93
	v_log_f32_e32 v28, v28
	v_exp_f32_e32 v27, v27
	v_sub_f32_e32 v26, v2, v26
	v_min_f32_e32 v2, 0, v3
	v_mul_f32_e32 v3, 0x3f317217, v28
	v_fma_f32 v3, v28, s95, -v3
	v_fmac_f32_e32 v3, 0x3377d1cf, v28
	v_fmac_f32_e32 v3, 0x3f317217, v28
	v_add_f32_e32 v27, 1.0, v27
	v_mul_f32_e64 v29, |v5|, s93
	v_exp_f32_e32 v29, v29
	v_log_f32_e32 v28, v27
	v_sub_f32_e32 v27, v2, v3
	v_min_f32_e32 v3, 0, v4
	v_add_f32_e32 v29, 1.0, v29
	v_mul_f32_e32 v4, 0x3f317217, v28
	v_fma_f32 v4, v28, s95, -v4
	v_fmac_f32_e32 v4, 0x3377d1cf, v28
	v_fmac_f32_e32 v4, 0x3f317217, v28
	v_mul_f32_e32 v2, 0x3d800000, v27
	v_fmac_f32_e32 v2, 0x3d800000, v26
	v_sub_f32_e32 v28, v3, v4
	v_log_f32_e32 v29, v29
	v_min_f32_e32 v3, 0, v5
	v_add_f32_e32 v5, v90, v6
	v_mul_f32_e64 v6, |v5|, s93
	v_exp_f32_e32 v6, v6
	v_mul_f32_e32 v4, 0x3f317217, v29
	v_fma_f32 v4, v29, s95, -v4
	v_fmac_f32_e32 v4, 0x3377d1cf, v29
	v_fmac_f32_e32 v4, 0x3f317217, v29
	v_add_f32_e32 v6, 1.0, v6
	v_mul_f32_e64 v30, |v7|, s93
	v_exp_f32_e32 v30, v30
	v_log_f32_e32 v6, v6
	v_sub_f32_e32 v29, v3, v4
	v_min_f32_e32 v4, 0, v5
	v_add_f32_e32 v30, 1.0, v30
	v_mul_f32_e32 v5, 0x3f317217, v6
	v_fma_f32 v5, v6, s95, -v5
	v_fmac_f32_e32 v5, 0x3377d1cf, v6
	v_fmac_f32_e32 v5, 0x3f317217, v6
	v_mul_f32_e32 v3, 0x3d800000, v29
	v_fmac_f32_e32 v3, 0x3d800000, v28
	v_add_f32_e32 v6, v90, v8
	v_log_f32_e32 v31, v30
	v_sub_f32_e32 v30, v4, v5
	v_min_f32_e32 v4, 0, v7
	v_mul_f32_e64 v7, |v6|, s93
	v_exp_f32_e32 v7, v7
	v_mul_f32_e32 v5, 0x3f317217, v31
	v_fma_f32 v5, v31, s95, -v5
	v_fmac_f32_e32 v5, 0x3377d1cf, v31
	v_fmac_f32_e32 v5, 0x3f317217, v31
	v_add_f32_e32 v7, 1.0, v7
	v_sub_f32_e32 v31, v4, v5
	v_log_f32_e32 v7, v7
	v_min_f32_e32 v4, 0, v6
	v_add_f32_e32 v6, v90, v9
	v_mul_f32_e64 v8, |v6|, s93
	v_exp_f32_e32 v8, v8
	v_mul_f32_e32 v5, 0x3f317217, v7
	v_fma_f32 v5, v7, s95, -v5
	v_fmac_f32_e32 v5, 0x3377d1cf, v7
	v_fmac_f32_e32 v5, 0x3f317217, v7
	v_add_f32_e32 v8, 1.0, v8
	v_add_f32_e32 v42, v2, v3
	v_sub_f32_e32 v32, v4, v5
	v_log_f32_e32 v8, v8
	v_min_f32_e32 v4, 0, v6
	v_add_f32_e32 v6, v90, v10
	v_mul_f32_e64 v7, |v6|, s93
	v_exp_f32_e32 v7, v7
	v_mul_f32_e32 v5, 0x3f317217, v8
	v_fma_f32 v5, v8, s95, -v5
	v_fmac_f32_e32 v5, 0x3377d1cf, v8
	v_fmac_f32_e32 v5, 0x3f317217, v8
	v_add_f32_e32 v7, 1.0, v7
	v_lshlrev_b32_e32 v2, 16, v52
	v_sub_f32_e32 v33, v4, v5
	v_log_f32_e32 v7, v7
	v_min_f32_e32 v4, 0, v6
	v_add_f32_e32 v6, v90, v11
	v_mul_f32_e64 v8, |v6|, s93
	v_exp_f32_e32 v8, v8
	v_mul_f32_e32 v5, 0x3f317217, v7
	v_fma_f32 v5, v7, s95, -v5
	v_fmac_f32_e32 v5, 0x3377d1cf, v7
	v_fmac_f32_e32 v5, 0x3f317217, v7
	v_add_f32_e32 v8, 1.0, v8
	v_and_b32_e32 v3, 0xffff0000, v52
	v_sub_f32_e32 v34, v4, v5
	v_log_f32_e32 v8, v8
	v_min_f32_e32 v4, 0, v6
	v_add_f32_e32 v6, v90, v12
	v_mul_f32_e64 v7, |v6|, s93
	v_exp_f32_e32 v7, v7
	v_mul_f32_e32 v5, 0x3f317217, v8
	v_fma_f32 v5, v8, s95, -v5
	v_fmac_f32_e32 v5, 0x3377d1cf, v8
	v_fmac_f32_e32 v5, 0x3f317217, v8
	v_add_f32_e32 v7, 1.0, v7
	v_pk_add_f32 v[2:3], v[44:45], v[2:3] neg_lo:[0,1] neg_hi:[0,1]
	v_sub_f32_e32 v35, v4, v5
	v_log_f32_e32 v7, v7
	v_min_f32_e32 v4, 0, v6
	v_add_f32_e32 v6, v90, v13
	v_mul_f32_e64 v8, |v6|, s93
	v_exp_f32_e32 v8, v8
	v_mul_f32_e32 v5, 0x3f317217, v7
	v_fma_f32 v5, v7, s95, -v5
	v_fmac_f32_e32 v5, 0x3377d1cf, v7
	v_fmac_f32_e32 v5, 0x3f317217, v7
	v_add_f32_e32 v8, 1.0, v8
	v_cvt_pk_bf16_f32 v44, v2, v3
	v_sub_f32_e32 v36, v4, v5
	v_log_f32_e32 v8, v8
	v_min_f32_e32 v4, 0, v6
	v_add_f32_e32 v6, v90, v14
	v_mul_f32_e64 v7, |v6|, s93
	v_exp_f32_e32 v7, v7
	v_mul_f32_e32 v5, 0x3f317217, v8
	v_fma_f32 v5, v8, s95, -v5
	v_fmac_f32_e32 v5, 0x3377d1cf, v8
	v_fmac_f32_e32 v5, 0x3f317217, v8
	v_add_f32_e32 v7, 1.0, v7
	v_cvt_pk_bf16_f32 v45, v46, v47
	v_sub_f32_e32 v37, v4, v5
	v_log_f32_e32 v7, v7
	v_min_f32_e32 v4, 0, v6
	v_add_f32_e32 v6, v90, v15
	v_mul_f32_e64 v8, |v6|, s93
	v_exp_f32_e32 v8, v8
	v_mul_f32_e32 v5, 0x3f317217, v7
	v_fma_f32 v5, v7, s95, -v5
	v_fmac_f32_e32 v5, 0x3377d1cf, v7
	v_fmac_f32_e32 v5, 0x3f317217, v7
	v_add_f32_e32 v8, 1.0, v8
	v_lshlrev_b32_e32 v46, 16, v54
	v_sub_f32_e32 v38, v4, v5
	v_log_f32_e32 v8, v8
	v_min_f32_e32 v4, 0, v6
	v_add_f32_e32 v6, v90, v16
	v_mul_f32_e64 v7, |v6|, s93
	v_exp_f32_e32 v7, v7
	v_mul_f32_e32 v5, 0x3f317217, v8
	v_fma_f32 v5, v8, s95, -v5
	v_fmac_f32_e32 v5, 0x3377d1cf, v8
	v_fmac_f32_e32 v5, 0x3f317217, v8
	v_add_f32_e32 v7, 1.0, v7
	v_and_b32_e32 v47, 0xffff0000, v54
	v_sub_f32_e32 v39, v4, v5
	v_log_f32_e32 v7, v7
	v_min_f32_e32 v4, 0, v6
	v_add_f32_e32 v6, v90, v17
	v_mul_f32_e64 v8, |v6|, s93
	v_exp_f32_e32 v8, v8
	v_mul_f32_e32 v5, 0x3f317217, v7
	v_fma_f32 v5, v7, s95, -v5
	v_fmac_f32_e32 v5, 0x3377d1cf, v7
	v_fmac_f32_e32 v5, 0x3f317217, v7
	v_add_f32_e32 v8, 1.0, v8
	v_pk_add_f32 v[46:47], v[48:49], v[46:47] neg_lo:[0,1] neg_hi:[0,1]
	v_sub_f32_e32 v40, v4, v5
	v_log_f32_e32 v8, v8
	v_min_f32_e32 v4, 0, v6
	v_lshlrev_b32_e32 v48, 16, v55
	v_mul_f32_e32 v5, 0x3f317217, v8
	v_fma_f32 v5, v8, s95, -v5
	v_fmac_f32_e32 v5, 0x3377d1cf, v8
	v_fmac_f32_e32 v5, 0x3f317217, v8
	v_and_b32_e32 v49, 0xffff0000, v55
	v_cvt_pk_bf16_f32 v46, v46, v47
	v_sub_f32_e32 v41, v4, v5
	v_mfma_f32_32x32x16_bf16 v[2:17], v[52:55], v[18:21], 0
	v_mul_f32_e32 v43, 0x3d800000, v31
	v_mul_f32_e32 v58, 0x3d800000, v33
	v_fmac_f32_e32 v43, 0x3d800000, v30
	v_fmac_f32_e32 v58, 0x3d800000, v32
	v_mul_f32_e32 v59, 0x3d800000, v35
	v_mul_f32_e32 v60, 0x3d800000, v37
	v_fmac_f32_e32 v59, 0x3d800000, v34
	v_mfma_f32_32x32x16_bf16 v[2:17], v[52:55], v[22:25], v[2:17]
	v_add_f32_e64 v22, v50, -v48
	v_add_f32_e64 v23, v51, -v49
	v_fmac_f32_e32 v60, 0x3d800000, v36
	v_cvt_pk_bf16_f32 v47, v22, v23
	v_add_f32_e32 v22, v43, v58
	v_mul_f32_e32 v61, 0x3d800000, v39
	v_mul_f32_e32 v62, 0x3d800000, v41
	v_fmac_f32_e32 v61, 0x3d800000, v38
	v_mfma_f32_32x32x16_bf16 v[2:17], v[44:47], v[18:21], v[2:17]
	v_add_f32_e32 v19, v59, v60
	v_fmac_f32_e32 v62, 0x3d800000, v40
	v_add_f32_e32 v21, v61, v62
	s_nop 8
	v_add_f32_e32 v2, v90, v2
	v_mul_f32_e64 v18, |v2|, s93
	v_exp_f32_e32 v18, v18
	v_add_f32_e32 v3, v90, v3
	v_mul_f32_e64 v23, |v3|, s93
	v_exp_f32_e32 v23, v23
	v_add_f32_e32 v18, 1.0, v18
	v_add_f32_e32 v4, v90, v4
	v_add_f32_e32 v23, 1.0, v23
	v_log_f32_e32 v18, v18
	v_min_f32_e32 v2, 0, v2
	v_add_f32_e32 v5, v90, v5
	v_add_f32_e32 v6, v90, v6
	v_mul_f32_e32 v20, 0x3f317217, v18
	v_fma_f32 v20, v18, s95, -v20
	v_fmac_f32_e32 v20, 0x3377d1cf, v18
	v_fmac_f32_e32 v20, 0x3f317217, v18
	v_add_f32_e32 v7, v90, v7
	v_add_f32_e32 v8, v90, v8
	v_mov_b32_e32 v18, v20
	v_mul_f32_e64 v20, |v4|, s93
	v_log_f32_e32 v23, v23
	v_exp_f32_e32 v20, v20
	v_sub_f32_e32 v2, v2, v18
	v_mul_f32_e64 v24, |v5|, s93
	v_mul_f32_e32 v18, 0x3f317217, v23
	v_fma_f32 v18, v23, s95, -v18
	v_fmac_f32_e32 v18, 0x3377d1cf, v23
	v_fmac_f32_e32 v18, 0x3f317217, v23
	v_add_f32_e32 v20, 1.0, v20
	v_exp_f32_e32 v24, v24
	s_nop 0
	v_add_f32_e32 v24, 1.0, v24
	v_log_f32_e32 v20, v20
	v_min_f32_e32 v4, 0, v4
	v_add_f32_e32 v9, v90, v9
	v_add_f32_e32 v10, v90, v10
	v_mul_f32_e32 v23, 0x3f317217, v20
	v_fma_f32 v23, v20, s95, -v23
	v_fmac_f32_e32 v23, 0x3377d1cf, v20
	v_fmac_f32_e32 v23, 0x3f317217, v20
	v_add_f32_e32 v11, v90, v11
	v_add_f32_e32 v12, v90, v12
	v_mov_b32_e32 v20, v23
	v_mul_f32_e64 v23, |v6|, s93
	v_log_f32_e32 v24, v24
	v_exp_f32_e32 v23, v23
	v_sub_f32_e32 v4, v4, v20
	v_mul_f32_e64 v25, |v7|, s93
	v_mul_f32_e32 v20, 0x3f317217, v24
	v_fma_f32 v20, v24, s95, -v20
	v_fmac_f32_e32 v20, 0x3377d1cf, v24
	v_fmac_f32_e32 v20, 0x3f317217, v24
	v_add_f32_e32 v23, 1.0, v23
	v_exp_f32_e32 v25, v25
	s_nop 0
	v_add_f32_e32 v25, 1.0, v25
	v_log_f32_e32 v23, v23
	v_min_f32_e32 v6, 0, v6
	v_add_f32_e32 v13, v90, v13
	v_add_f32_e32 v15, v90, v15
	v_mul_f32_e32 v24, 0x3f317217, v23
	v_fma_f32 v24, v23, s95, -v24
	v_fmac_f32_e32 v24, 0x3377d1cf, v23
	v_fmac_f32_e32 v24, 0x3f317217, v23
	v_min_f32_e32 v7, 0, v7
	v_min_f32_e32 v3, 0, v3
	v_mov_b32_e32 v23, v24
	v_mul_f32_e64 v24, |v8|, s93
	v_log_f32_e32 v25, v25
	v_exp_f32_e32 v24, v24
	v_sub_f32_e32 v6, v6, v23
	v_mul_f32_e64 v43, |v9|, s93
	v_mul_f32_e32 v23, 0x3f317217, v25
	v_fma_f32 v23, v25, s95, -v23
	v_fmac_f32_e32 v23, 0x3377d1cf, v25
	v_fmac_f32_e32 v23, 0x3f317217, v25
	v_add_f32_e32 v24, 1.0, v24
	v_exp_f32_e32 v43, v43
	s_nop 0
	v_add_f32_e32 v43, 1.0, v43
	v_log_f32_e32 v24, v24
	v_min_f32_e32 v8, 0, v8
	v_min_f32_e32 v9, 0, v9
	v_sub_f32_e32 v7, v7, v23
	v_mul_f32_e32 v25, 0x3f317217, v24
	v_fma_f32 v25, v24, s95, -v25
	v_fmac_f32_e32 v25, 0x3377d1cf, v24
	v_fmac_f32_e32 v25, 0x3f317217, v24
	v_mul_f32_e32 v23, 0x3d800000, v7
	v_fmac_f32_e32 v23, 0x3d800000, v6
	v_mov_b32_e32 v24, v25
	v_mul_f32_e64 v25, |v10|, s93
	v_log_f32_e32 v43, v43
	v_exp_f32_e32 v25, v25
	v_sub_f32_e32 v8, v8, v24
	v_mul_f32_e64 v44, |v11|, s93
	v_mul_f32_e32 v24, 0x3f317217, v43
	v_fma_f32 v24, v43, s95, -v24
	v_fmac_f32_e32 v24, 0x3377d1cf, v43
	v_fmac_f32_e32 v24, 0x3f317217, v43
	v_add_f32_e32 v25, 1.0, v25
	v_exp_f32_e32 v44, v44
	s_nop 0
	v_add_f32_e32 v44, 1.0, v44
	v_log_f32_e32 v25, v25
	v_min_f32_e32 v10, 0, v10
	v_sub_f32_e32 v9, v9, v24
	v_mul_f32_e32 v24, 0x3d800000, v9
	v_mul_f32_e32 v43, 0x3f317217, v25
	v_fma_f32 v43, v25, s95, -v43
	v_fmac_f32_e32 v43, 0x3377d1cf, v25
	v_fmac_f32_e32 v43, 0x3f317217, v25
	v_fmac_f32_e32 v24, 0x3d800000, v8
	v_add_f32_e32 v23, v23, v24
	v_mov_b32_e32 v25, v43
	v_mul_f32_e64 v43, |v12|, s93
	v_log_f32_e32 v44, v44
	v_exp_f32_e32 v43, v43
	v_sub_f32_e32 v25, v10, v25
	v_min_f32_e32 v10, 0, v11
	v_mul_f32_e32 v11, 0x3f317217, v44
	v_fma_f32 v11, v44, s95, -v11
	v_fmac_f32_e32 v11, 0x3377d1cf, v44
	v_fmac_f32_e32 v11, 0x3f317217, v44
	v_add_f32_e32 v43, 1.0, v43
	v_mul_f32_e64 v45, |v13|, s93
	v_exp_f32_e32 v45, v45
	v_log_f32_e32 v43, v43
	v_sub_f32_e32 v44, v10, v11
	v_min_f32_e32 v11, 0, v12
	v_add_f32_e32 v45, 1.0, v45
	v_mul_f32_e32 v12, 0x3f317217, v43
	v_fma_f32 v12, v43, s95, -v12
	v_fmac_f32_e32 v12, 0x3377d1cf, v43
	v_fmac_f32_e32 v12, 0x3f317217, v43
	v_mul_f32_e32 v10, 0x3d800000, v44
	v_fmac_f32_e32 v10, 0x3d800000, v25
	v_sub_f32_e32 v43, v11, v12
	v_log_f32_e32 v45, v45
	v_min_f32_e32 v11, 0, v13
	v_add_f32_e32 v13, v90, v14
	v_mul_f32_e64 v14, |v13|, s93
	v_exp_f32_e32 v14, v14
	v_mul_f32_e32 v12, 0x3f317217, v45
	v_fma_f32 v12, v45, s95, -v12
	v_fmac_f32_e32 v12, 0x3377d1cf, v45
	v_fmac_f32_e32 v12, 0x3f317217, v45
	v_add_f32_e32 v14, 1.0, v14
	v_mul_f32_e64 v46, |v15|, s93
	v_exp_f32_e32 v46, v46
	v_log_f32_e32 v14, v14
	v_sub_f32_e32 v45, v11, v12
	v_min_f32_e32 v12, 0, v13
	v_add_f32_e32 v46, 1.0, v46
	v_mul_f32_e32 v13, 0x3f317217, v14
	v_fma_f32 v13, v14, s95, -v13
	v_fmac_f32_e32 v13, 0x3377d1cf, v14
	v_fmac_f32_e32 v13, 0x3f317217, v14
	v_mul_f32_e32 v11, 0x3d800000, v45
	v_fmac_f32_e32 v11, 0x3d800000, v43
	v_add_f32_e32 v14, v90, v16
	v_log_f32_e32 v46, v46
	v_sub_f32_e32 v47, v12, v13
	v_min_f32_e32 v12, 0, v15
	v_mul_f32_e64 v15, |v14|, s93
	v_exp_f32_e32 v15, v15
	v_mul_f32_e32 v13, 0x3f317217, v46
	v_fma_f32 v13, v46, s95, -v13
	v_fmac_f32_e32 v13, 0x3377d1cf, v46
	v_fmac_f32_e32 v13, 0x3f317217, v46
	v_add_f32_e32 v15, 1.0, v15
	v_sub_f32_e32 v46, v12, v13
	v_log_f32_e32 v15, v15
	v_add_f32_e32 v16, v90, v17
	v_mul_f32_e64 v17, |v16|, s93
	v_exp_f32_e32 v17, v17
	v_min_f32_e32 v13, 0, v14
	v_mul_f32_e32 v14, 0x3f317217, v15
	v_fma_f32 v14, v15, s95, -v14
	v_fmac_f32_e32 v14, 0x3377d1cf, v15
	v_fmac_f32_e32 v14, 0x3f317217, v15
	v_add_f32_e32 v17, 1.0, v17
	v_add_f32_e32 v24, v10, v11
	v_mul_f32_e32 v12, 0x3d800000, v46
	v_log_f32_e32 v17, v17
	v_sub_f32_e32 v48, v13, v14
	v_min_f32_e32 v13, 0, v16
	v_mul_f32_e32 v14, 0x3f317217, v17
	v_fma_f32 v14, v17, s95, -v14
	v_fmac_f32_e32 v14, 0x3377d1cf, v17
	v_fmac_f32_e32 v14, 0x3f317217, v17
	v_fmac_f32_e32 v12, 0x3d800000, v47
	v_min_f32_e32 v5, 0, v5
	v_sub_f32_e32 v49, v13, v14
	ds_bpermute_b32 v14, v1, v42
	v_mul_f32_e32 v13, 0x3d800000, v49
	v_fmac_f32_e32 v13, 0x3d800000, v48
	v_add_f32_e32 v51, v12, v13
	v_sub_f32_e32 v3, v3, v18
	s_waitcnt lgkmcnt(0)
	v_add_f32_e32 v10, 0, v14
	v_cndmask_b32_e64 v52, v10, 0, s[4:5]
	ds_bpermute_b32 v10, v1, v22
	v_fmac_f32_e32 v52, 0x3d800000, v26
	v_fmamk_f32 v26, v27, 0x3d800000, v52
	v_add_f32_e32 v11, v42, v14
	v_fmamk_f32 v27, v28, 0x3d800000, v26
	v_add_f32_e32 v11, 0, v11
	s_waitcnt lgkmcnt(0)
	v_cndmask_b32_e64 v12, v10, 0, s[4:5]
	v_fmamk_f32 v28, v29, 0x3d800000, v27
	v_add_f32_e32 v29, v12, v11
	ds_bpermute_b32 v12, v1, v19
	v_add_f32_e32 v10, v22, v10
	v_add_f32_e32 v10, v10, v11
	v_sub_f32_e32 v5, v5, v20
	v_fmac_f32_e32 v29, 0x3d800000, v30
	s_waitcnt lgkmcnt(0)
	v_cndmask_b32_e64 v11, v12, 0, s[4:5]
	v_add_f32_e32 v22, v11, v10
	ds_bpermute_b32 v11, v1, v21
	v_mul_f32_e32 v18, 0x3d800000, v3
	v_mul_f32_e32 v20, 0x3d800000, v5
	v_fmamk_f32 v30, v31, 0x3d800000, v29
	v_fmac_f32_e32 v18, 0x3d800000, v2
	v_fmac_f32_e32 v20, 0x3d800000, v4
	v_fmamk_f32 v31, v32, 0x3d800000, v30
	v_fmac_f32_e32 v22, 0x3d800000, v34
	v_add_f32_e32 v12, v19, v12
	v_add_f32_e32 v50, v18, v20
	v_fmamk_f32 v32, v33, 0x3d800000, v31
	v_fmamk_f32 v33, v35, 0x3d800000, v22
	v_add_f32_e32 v10, v12, v10
	s_waitcnt lgkmcnt(0)
	v_cndmask_b32_e64 v12, v11, 0, s[4:5]
	v_fmamk_f32 v34, v36, 0x3d800000, v33
	v_add_f32_e32 v36, v12, v10
	ds_bpermute_b32 v12, v1, v50
	v_add_f32_e32 v11, v21, v11
	v_add_f32_e32 v10, v11, v10
	v_fmac_f32_e32 v36, 0x3d800000, v38
	v_mul_f32_e32 v21, 0x3fb8aa3b, v52
	s_waitcnt lgkmcnt(0)
	v_cndmask_b32_e64 v11, v12, 0, s[4:5]
	v_add_f32_e32 v17, v11, v10
	v_fmac_f32_e32 v17, 0x3d800000, v2
	ds_bpermute_b32 v2, v1, v23
	v_fmamk_f32 v16, v3, 0x3d800000, v17
	v_add_f32_e32 v3, v50, v12
	v_fmamk_f32 v15, v4, 0x3d800000, v16
	v_add_f32_e32 v3, v10, v3
	s_waitcnt lgkmcnt(0)
	v_cndmask_b32_e64 v4, v2, 0, s[4:5]
	v_add_f32_e32 v13, v4, v3
	ds_bpermute_b32 v4, v1, v24
	v_fmac_f32_e32 v13, 0x3d800000, v6
	v_fmamk_f32 v12, v7, 0x3d800000, v13
	v_add_f32_e32 v2, v23, v2
	v_fmamk_f32 v11, v8, 0x3d800000, v12
	v_add_f32_e32 v2, v2, v3
	s_waitcnt lgkmcnt(0)
	v_cndmask_b32_e64 v3, v4, 0, s[4:5]
	v_fmamk_f32 v10, v9, 0x3d800000, v11
	v_add_f32_e32 v9, v3, v2
	ds_bpermute_b32 v3, v1, v51
	v_fmamk_f32 v20, v39, 0x3d800000, v36
	v_exp_f32_e32 v21, v21
	v_fmamk_f32 v19, v40, 0x3d800000, v20
	v_add_f32_e32 v4, v24, v4
	v_fmamk_f32 v35, v37, 0x3d800000, v34
	v_fmamk_f32 v18, v41, 0x3d800000, v19
	v_fmac_f32_e32 v9, 0x3d800000, v25
	v_add_f32_e32 v2, v4, v2
	s_waitcnt lgkmcnt(0)
	v_cndmask_b32_e64 v3, v3, 0, s[4:5]
	ds_read_u16 v23, v188 offset:6144
	ds_read_u16 v24, v188 offset:6288
	ds_read_u16 v25, v188 offset:6432
	ds_read_u16 v37, v188 offset:6576
	ds_read_u16 v38, v188 offset:7296
	ds_read_u16 v39, v188 offset:7440
	ds_read_u16 v40, v188 offset:7584
	ds_read_u16 v41, v188 offset:7728
	v_fmamk_f32 v14, v5, 0x3d800000, v15
	v_add_f32_e32 v5, v3, v2
	s_waitcnt lgkmcnt(7)
	v_lshlrev_b32_e32 v23, 16, v23
	v_fmac_f32_e32 v5, 0x3d800000, v47
	v_mul_f32_e32 v21, v21, v23
	v_mul_f32_e32 v23, 0xbfb8aa3b, v52
	v_fmamk_f32 v8, v44, 0x3d800000, v9
	v_fmamk_f32 v4, v46, 0x3d800000, v5
	v_exp_f32_e32 v23, v23
	v_fmamk_f32 v7, v43, 0x3d800000, v8
	v_fmamk_f32 v3, v48, 0x3d800000, v4
	v_fmamk_f32 v6, v45, 0x3d800000, v7
	v_fmamk_f32 v2, v49, 0x3d800000, v3
	ds_read_u16 v42, v188 offset:43008
	ds_read_u16 v43, v188 offset:43152
	ds_read_u16 v44, v188 offset:43296
	ds_read_u16 v45, v188 offset:43440
	ds_read_u16 v46, v188 offset:44160
	ds_read_u16 v47, v188 offset:44304
	ds_read_u16 v48, v188 offset:44448
	ds_read_u16 v49, v188 offset:44592
	v_mul_f32_e32 v21, 0x3e000000, v21
	s_waitcnt lgkmcnt(7)
	v_lshlrev_b32_e32 v42, 16, v42
	v_mul_f32_e32 v23, v23, v42
	v_bfe_u32 v42, v21, 16, 1
	v_add3_u32 v21, v21, v42, s97
	ds_write_b16_d16_hi v188, v21 offset:6144
	v_bfe_u32 v21, v23, 16, 1
	v_add3_u32 v21, v23, v21, s97
	ds_write_b16_d16_hi v188, v21 offset:43008
	v_mul_f32_e32 v21, 0x3fb8aa3b, v26
	v_exp_f32_e32 v21, v21
	v_lshlrev_b32_e32 v23, 16, v24
	v_mul_f32_e32 v24, 0xbfb8aa3b, v26
	v_exp_f32_e32 v24, v24
	v_mul_f32_e32 v21, v21, v23
	v_mul_f32_e32 v21, 0x3e000000, v21
	s_waitcnt lgkmcnt(8)
	v_lshlrev_b32_e32 v23, 16, v43
	v_mul_f32_e32 v23, v24, v23
	v_bfe_u32 v24, v21, 16, 1
	v_add3_u32 v21, v21, v24, s97
	ds_write_b16_d16_hi v188, v21 offset:6288
	v_bfe_u32 v21, v23, 16, 1
	v_add3_u32 v21, v23, v21, s97
	ds_write_b16_d16_hi v188, v21 offset:43152
	v_mul_f32_e32 v21, 0x3fb8aa3b, v27
	v_exp_f32_e32 v21, v21
	v_mul_f32_e32 v24, 0xbfb8aa3b, v27
	v_exp_f32_e32 v24, v24
	v_lshlrev_b32_e32 v23, 16, v25
	v_mul_f32_e32 v21, v21, v23
	v_mul_f32_e32 v21, 0x3e000000, v21
	s_waitcnt lgkmcnt(9)
	v_lshlrev_b32_e32 v23, 16, v44
	v_mul_f32_e32 v23, v24, v23
	v_bfe_u32 v24, v21, 16, 1
	v_add3_u32 v21, v21, v24, s97
	ds_write_b16_d16_hi v188, v21 offset:6432
	v_bfe_u32 v21, v23, 16, 1
	v_add3_u32 v21, v23, v21, s97
	ds_write_b16_d16_hi v188, v21 offset:43296
	v_mul_f32_e32 v21, 0x3fb8aa3b, v28
	v_exp_f32_e32 v21, v21
	v_mul_f32_e32 v24, 0xbfb8aa3b, v28
	v_exp_f32_e32 v24, v24
	v_lshlrev_b32_e32 v23, 16, v37
	v_mul_f32_e32 v21, v21, v23
	v_mul_f32_e32 v21, 0x3e000000, v21
	s_waitcnt lgkmcnt(10)
	v_lshlrev_b32_e32 v23, 16, v45
	v_mul_f32_e32 v23, v24, v23
	v_bfe_u32 v24, v21, 16, 1
	v_add3_u32 v21, v21, v24, s97
	ds_write_b16_d16_hi v188, v21 offset:6576
	v_bfe_u32 v21, v23, 16, 1
	v_add3_u32 v21, v23, v21, s97
	ds_write_b16_d16_hi v188, v21 offset:43440
	v_mul_f32_e32 v21, 0x3fb8aa3b, v29
	v_exp_f32_e32 v21, v21
	v_mul_f32_e32 v24, 0xbfb8aa3b, v29
	v_exp_f32_e32 v24, v24
	v_lshlrev_b32_e32 v23, 16, v38
	v_mul_f32_e32 v21, v21, v23
	v_mul_f32_e32 v21, 0x3e000000, v21
	s_waitcnt lgkmcnt(11)
	v_lshlrev_b32_e32 v23, 16, v46
	v_mul_f32_e32 v23, v24, v23
	v_bfe_u32 v24, v21, 16, 1
	v_add3_u32 v21, v21, v24, s97
	ds_write_b16_d16_hi v188, v21 offset:7296
	v_bfe_u32 v21, v23, 16, 1
	v_add3_u32 v21, v23, v21, s97
	ds_write_b16_d16_hi v188, v21 offset:44160
	v_mul_f32_e32 v21, 0x3fb8aa3b, v30
	v_exp_f32_e32 v21, v21
	v_mul_f32_e32 v24, 0xbfb8aa3b, v30
	v_exp_f32_e32 v24, v24
	v_lshlrev_b32_e32 v23, 16, v39
	v_mul_f32_e32 v21, v21, v23
	v_mul_f32_e32 v21, 0x3e000000, v21
	s_waitcnt lgkmcnt(12)
	v_lshlrev_b32_e32 v23, 16, v47
	v_mul_f32_e32 v23, v24, v23
	v_bfe_u32 v24, v21, 16, 1
	v_add3_u32 v21, v21, v24, s97
	ds_write_b16_d16_hi v188, v21 offset:7440
	v_bfe_u32 v21, v23, 16, 1
	v_add3_u32 v21, v23, v21, s97
	ds_write_b16_d16_hi v188, v21 offset:44304
	v_mul_f32_e32 v21, 0x3fb8aa3b, v31
	v_exp_f32_e32 v21, v21
	v_mul_f32_e32 v24, 0xbfb8aa3b, v31
	v_exp_f32_e32 v24, v24
	v_lshlrev_b32_e32 v23, 16, v40
	v_mul_f32_e32 v21, v21, v23
	v_mul_f32_e32 v21, 0x3e000000, v21
	s_waitcnt lgkmcnt(13)
	v_lshlrev_b32_e32 v23, 16, v48
	v_mul_f32_e32 v23, v24, v23
	v_bfe_u32 v24, v21, 16, 1
	v_add3_u32 v21, v21, v24, s97
	ds_write_b16_d16_hi v188, v21 offset:7584
	v_bfe_u32 v21, v23, 16, 1
	v_add3_u32 v21, v23, v21, s97
	ds_write_b16_d16_hi v188, v21 offset:44448
	v_mul_f32_e32 v21, 0x3fb8aa3b, v32
	v_exp_f32_e32 v21, v21
	v_mul_f32_e32 v24, 0xbfb8aa3b, v32
	v_exp_f32_e32 v24, v24
	v_lshlrev_b32_e32 v23, 16, v41
	v_mul_f32_e32 v21, v21, v23
	v_mul_f32_e32 v21, 0x3e000000, v21
	s_waitcnt lgkmcnt(14)
	v_lshlrev_b32_e32 v23, 16, v49
	v_mul_f32_e32 v23, v24, v23
	v_bfe_u32 v24, v21, 16, 1
	v_add3_u32 v21, v21, v24, s97
	ds_write_b16_d16_hi v188, v21 offset:7728
	v_bfe_u32 v21, v23, 16, 1
	v_add3_u32 v21, v23, v21, s97
	ds_write_b16_d16_hi v188, v21 offset:44592
	v_mul_f32_e32 v21, 0x3fb8aa3b, v22
	v_exp_f32_e32 v21, v21
	v_mul_f32_e32 v22, 0xbfb8aa3b, v22
	ds_read_u16 v23, v188 offset:8448
	ds_read_u16 v24, v188 offset:8592
	ds_read_u16 v25, v188 offset:8736
	ds_read_u16 v26, v188 offset:8880
	ds_read_u16 v27, v188 offset:9600
	ds_read_u16 v28, v188 offset:9744
	ds_read_u16 v29, v188 offset:9888
	ds_read_u16 v30, v188 offset:10032
	v_exp_f32_e32 v22, v22
	s_waitcnt lgkmcnt(7)
	v_lshlrev_b32_e32 v23, 16, v23
	v_mul_f32_e32 v21, v21, v23
	ds_read_u16 v23, v188 offset:45312
	ds_read_u16 v31, v188 offset:45456
	ds_read_u16 v32, v188 offset:45600
	ds_read_u16 v37, v188 offset:45744
	ds_read_u16 v38, v188 offset:46464
	ds_read_u16 v39, v188 offset:46608
	ds_read_u16 v40, v188 offset:46752
	ds_read_u16 v41, v188 offset:46896
	v_mul_f32_e32 v21, 0x3e000000, v21
	s_waitcnt lgkmcnt(7)
	v_lshlrev_b32_e32 v23, 16, v23
	v_mul_f32_e32 v22, v22, v23
	v_bfe_u32 v23, v21, 16, 1
	v_add3_u32 v21, v21, v23, s97
	ds_write_b16_d16_hi v188, v21 offset:8448
	v_bfe_u32 v21, v22, 16, 1
	v_add3_u32 v21, v22, v21, s97
	ds_write_b16_d16_hi v188, v21 offset:45312
	v_mul_f32_e32 v21, 0x3fb8aa3b, v33
	v_exp_f32_e32 v21, v21
	v_mul_f32_e32 v23, 0xbfb8aa3b, v33
	v_exp_f32_e32 v23, v23
	v_lshlrev_b32_e32 v22, 16, v24
	v_mul_f32_e32 v21, v21, v22
	v_mul_f32_e32 v21, 0x3e000000, v21
	s_waitcnt lgkmcnt(8)
	v_lshlrev_b32_e32 v22, 16, v31
	v_mul_f32_e32 v22, v23, v22
	v_bfe_u32 v23, v21, 16, 1
	v_add3_u32 v21, v21, v23, s97
	ds_write_b16_d16_hi v188, v21 offset:8592
	v_bfe_u32 v21, v22, 16, 1
	v_add3_u32 v21, v22, v21, s97
	ds_write_b16_d16_hi v188, v21 offset:45456
	v_mul_f32_e32 v21, 0x3fb8aa3b, v34
	v_exp_f32_e32 v21, v21
	v_mul_f32_e32 v23, 0xbfb8aa3b, v34
	v_exp_f32_e32 v23, v23
	v_lshlrev_b32_e32 v22, 16, v25
	v_mul_f32_e32 v21, v21, v22
	v_mul_f32_e32 v21, 0x3e000000, v21
	s_waitcnt lgkmcnt(9)
	v_lshlrev_b32_e32 v22, 16, v32
	v_mul_f32_e32 v22, v23, v22
	v_bfe_u32 v23, v21, 16, 1
	v_add3_u32 v21, v21, v23, s97
	ds_write_b16_d16_hi v188, v21 offset:8736
	v_bfe_u32 v21, v22, 16, 1
	v_add3_u32 v21, v22, v21, s97
	ds_write_b16_d16_hi v188, v21 offset:45600
	v_mul_f32_e32 v21, 0x3fb8aa3b, v35
	v_exp_f32_e32 v21, v21
	v_mul_f32_e32 v23, 0xbfb8aa3b, v35
	v_exp_f32_e32 v23, v23
	v_lshlrev_b32_e32 v22, 16, v26
	v_mul_f32_e32 v21, v21, v22
	v_mul_f32_e32 v21, 0x3e000000, v21
	s_waitcnt lgkmcnt(10)
	v_lshlrev_b32_e32 v22, 16, v37
	v_mul_f32_e32 v22, v23, v22
	v_bfe_u32 v23, v21, 16, 1
	v_add3_u32 v21, v21, v23, s97
	ds_write_b16_d16_hi v188, v21 offset:8880
	v_bfe_u32 v21, v22, 16, 1
	v_add3_u32 v21, v22, v21, s97
	ds_write_b16_d16_hi v188, v21 offset:45744
	v_mul_f32_e32 v21, 0x3fb8aa3b, v36
	v_exp_f32_e32 v21, v21
	v_mul_f32_e32 v23, 0xbfb8aa3b, v36
	v_exp_f32_e32 v23, v23
	v_lshlrev_b32_e32 v22, 16, v27
	v_mul_f32_e32 v21, v21, v22
	v_mul_f32_e32 v21, 0x3e000000, v21
	s_waitcnt lgkmcnt(11)
	v_lshlrev_b32_e32 v22, 16, v38
	v_mul_f32_e32 v22, v23, v22
	v_bfe_u32 v23, v21, 16, 1
	v_add3_u32 v21, v21, v23, s97
	ds_write_b16_d16_hi v188, v21 offset:9600
	v_bfe_u32 v21, v22, 16, 1
	v_add3_u32 v21, v22, v21, s97
	ds_write_b16_d16_hi v188, v21 offset:46464
	v_mul_f32_e32 v21, 0x3fb8aa3b, v20
	v_exp_f32_e32 v21, v21
	v_mul_f32_e32 v20, 0xbfb8aa3b, v20
	v_exp_f32_e32 v20, v20
	v_lshlrev_b32_e32 v22, 16, v28
	v_mul_f32_e32 v21, v21, v22
	v_mul_f32_e32 v21, 0x3e000000, v21
	s_waitcnt lgkmcnt(12)
	v_lshlrev_b32_e32 v22, 16, v39
	v_mul_f32_e32 v20, v20, v22
	v_bfe_u32 v22, v21, 16, 1
	v_add3_u32 v21, v21, v22, s97
	ds_write_b16_d16_hi v188, v21 offset:9744
	v_bfe_u32 v21, v20, 16, 1
	v_add3_u32 v20, v20, v21, s97
	ds_write_b16_d16_hi v188, v20 offset:46608
	v_mul_f32_e32 v20, 0x3fb8aa3b, v19
	v_exp_f32_e32 v20, v20
	v_mul_f32_e32 v19, 0xbfb8aa3b, v19
	v_exp_f32_e32 v19, v19
	v_lshlrev_b32_e32 v21, 16, v29
	v_mul_f32_e32 v20, v20, v21
	v_mul_f32_e32 v20, 0x3e000000, v20
	s_waitcnt lgkmcnt(13)
	v_lshlrev_b32_e32 v21, 16, v40
	v_mul_f32_e32 v19, v19, v21
	v_bfe_u32 v21, v20, 16, 1
	v_add3_u32 v20, v20, v21, s97
	ds_write_b16_d16_hi v188, v20 offset:9888
	v_bfe_u32 v20, v19, 16, 1
	v_add3_u32 v19, v19, v20, s97
	ds_write_b16_d16_hi v188, v19 offset:46752
	v_mul_f32_e32 v19, 0x3fb8aa3b, v18
	v_exp_f32_e32 v19, v19
	v_mul_f32_e32 v18, 0xbfb8aa3b, v18
	v_exp_f32_e32 v18, v18
	v_lshlrev_b32_e32 v20, 16, v30
	v_mul_f32_e32 v19, v19, v20
	v_mul_f32_e32 v19, 0x3e000000, v19
	s_waitcnt lgkmcnt(14)
	v_lshlrev_b32_e32 v20, 16, v41
	v_mul_f32_e32 v18, v18, v20
	v_bfe_u32 v20, v19, 16, 1
	v_add3_u32 v19, v19, v20, s97
	ds_write_b16_d16_hi v188, v19 offset:10032
	v_bfe_u32 v19, v18, 16, 1
	v_add3_u32 v18, v18, v19, s97
	ds_write_b16_d16_hi v188, v18 offset:46896
	v_mul_f32_e32 v18, 0x3fb8aa3b, v17
	v_exp_f32_e32 v18, v18
	v_mul_f32_e32 v17, 0xbfb8aa3b, v17
	ds_read_u16 v19, v188 offset:10752
	ds_read_u16 v20, v188 offset:10896
	ds_read_u16 v21, v188 offset:11040
	ds_read_u16 v22, v188 offset:11184
	ds_read_u16 v23, v188 offset:11904
	ds_read_u16 v24, v188 offset:12048
	ds_read_u16 v25, v188 offset:12192
	ds_read_u16 v26, v188 offset:12336
	v_exp_f32_e32 v17, v17
	s_waitcnt lgkmcnt(7)
	v_lshlrev_b32_e32 v19, 16, v19
	v_mul_f32_e32 v18, v18, v19
	ds_read_u16 v19, v188 offset:47616
	ds_read_u16 v27, v188 offset:47760
	ds_read_u16 v28, v188 offset:47904
	ds_read_u16 v29, v188 offset:48048
	ds_read_u16 v30, v188 offset:48768
	ds_read_u16 v31, v188 offset:48912
	ds_read_u16 v32, v188 offset:49056
	ds_read_u16 v33, v188 offset:49200
	v_mul_f32_e32 v18, 0x3e000000, v18
	s_waitcnt lgkmcnt(7)
	v_lshlrev_b32_e32 v19, 16, v19
	v_mul_f32_e32 v17, v17, v19
	v_bfe_u32 v19, v18, 16, 1
	v_add3_u32 v18, v18, v19, s97
	ds_write_b16_d16_hi v188, v18 offset:10752
	v_bfe_u32 v18, v17, 16, 1
	v_add3_u32 v17, v17, v18, s97
	ds_write_b16_d16_hi v188, v17 offset:47616
	v_mul_f32_e32 v17, 0x3fb8aa3b, v16
	v_exp_f32_e32 v17, v17
	v_mul_f32_e32 v16, 0xbfb8aa3b, v16
	v_exp_f32_e32 v16, v16
	v_lshlrev_b32_e32 v18, 16, v20
	v_mul_f32_e32 v17, v17, v18
	v_mul_f32_e32 v17, 0x3e000000, v17
	s_waitcnt lgkmcnt(8)
	v_lshlrev_b32_e32 v18, 16, v27
	v_mul_f32_e32 v16, v16, v18
	v_bfe_u32 v18, v17, 16, 1
	v_add3_u32 v17, v17, v18, s97
	ds_write_b16_d16_hi v188, v17 offset:10896
	v_bfe_u32 v17, v16, 16, 1
	v_add3_u32 v16, v16, v17, s97
	ds_write_b16_d16_hi v188, v16 offset:47760
	v_mul_f32_e32 v16, 0x3fb8aa3b, v15
	v_exp_f32_e32 v16, v16
	v_mul_f32_e32 v15, 0xbfb8aa3b, v15
	v_exp_f32_e32 v15, v15
	v_lshlrev_b32_e32 v17, 16, v21
	v_mul_f32_e32 v16, v16, v17
	v_mul_f32_e32 v16, 0x3e000000, v16
	s_waitcnt lgkmcnt(9)
	v_lshlrev_b32_e32 v17, 16, v28
	v_mul_f32_e32 v15, v15, v17
	v_bfe_u32 v17, v16, 16, 1
	v_add3_u32 v16, v16, v17, s97
	ds_write_b16_d16_hi v188, v16 offset:11040
	v_bfe_u32 v16, v15, 16, 1
	v_add3_u32 v15, v15, v16, s97
	ds_write_b16_d16_hi v188, v15 offset:47904
	v_mul_f32_e32 v15, 0x3fb8aa3b, v14
	v_exp_f32_e32 v15, v15
	v_mul_f32_e32 v14, 0xbfb8aa3b, v14
	v_exp_f32_e32 v14, v14
	v_lshlrev_b32_e32 v16, 16, v22
	v_mul_f32_e32 v15, v15, v16
	v_mul_f32_e32 v15, 0x3e000000, v15
	s_waitcnt lgkmcnt(10)
	v_lshlrev_b32_e32 v16, 16, v29
	v_mul_f32_e32 v14, v14, v16
	v_bfe_u32 v16, v15, 16, 1
	v_add3_u32 v15, v15, v16, s97
	ds_write_b16_d16_hi v188, v15 offset:11184
	v_bfe_u32 v15, v14, 16, 1
	v_add3_u32 v14, v14, v15, s97
	ds_write_b16_d16_hi v188, v14 offset:48048
	v_mul_f32_e32 v14, 0x3fb8aa3b, v13
	v_exp_f32_e32 v14, v14
	v_mul_f32_e32 v13, 0xbfb8aa3b, v13
	v_exp_f32_e32 v13, v13
	v_lshlrev_b32_e32 v15, 16, v23
	v_mul_f32_e32 v14, v14, v15
	v_mul_f32_e32 v14, 0x3e000000, v14
	s_waitcnt lgkmcnt(11)
	v_lshlrev_b32_e32 v15, 16, v30
	v_mul_f32_e32 v13, v13, v15
	v_bfe_u32 v15, v14, 16, 1
	v_add3_u32 v14, v14, v15, s97
	ds_write_b16_d16_hi v188, v14 offset:11904
	v_bfe_u32 v14, v13, 16, 1
	v_add3_u32 v13, v13, v14, s97
	ds_write_b16_d16_hi v188, v13 offset:48768
	v_mul_f32_e32 v13, 0x3fb8aa3b, v12
	v_exp_f32_e32 v13, v13
	v_mul_f32_e32 v12, 0xbfb8aa3b, v12
	v_exp_f32_e32 v12, v12
	v_lshlrev_b32_e32 v14, 16, v24
	v_mul_f32_e32 v13, v13, v14
	v_mul_f32_e32 v13, 0x3e000000, v13
	s_waitcnt lgkmcnt(12)
	v_lshlrev_b32_e32 v14, 16, v31
	v_mul_f32_e32 v12, v12, v14
	v_bfe_u32 v14, v13, 16, 1
	v_add3_u32 v13, v13, v14, s97
	ds_write_b16_d16_hi v188, v13 offset:12048
	v_bfe_u32 v13, v12, 16, 1
	v_add3_u32 v12, v12, v13, s97
	ds_write_b16_d16_hi v188, v12 offset:48912
	v_mul_f32_e32 v12, 0x3fb8aa3b, v11
	v_exp_f32_e32 v12, v12
	v_mul_f32_e32 v11, 0xbfb8aa3b, v11
	v_exp_f32_e32 v11, v11
	v_lshlrev_b32_e32 v13, 16, v25
	v_mul_f32_e32 v12, v12, v13
	v_mul_f32_e32 v12, 0x3e000000, v12
	s_waitcnt lgkmcnt(13)
	v_lshlrev_b32_e32 v13, 16, v32
	v_mul_f32_e32 v11, v11, v13
	v_bfe_u32 v13, v12, 16, 1
	v_add3_u32 v12, v12, v13, s97
	ds_write_b16_d16_hi v188, v12 offset:12192
	v_bfe_u32 v12, v11, 16, 1
	v_add3_u32 v11, v11, v12, s97
	ds_write_b16_d16_hi v188, v11 offset:49056
	v_mul_f32_e32 v11, 0x3fb8aa3b, v10
	v_exp_f32_e32 v11, v11
	v_mul_f32_e32 v10, 0xbfb8aa3b, v10
	v_exp_f32_e32 v10, v10
	v_lshlrev_b32_e32 v12, 16, v26
	v_mul_f32_e32 v11, v11, v12
	v_mul_f32_e32 v11, 0x3e000000, v11
	s_waitcnt lgkmcnt(14)
	v_lshlrev_b32_e32 v12, 16, v33
	v_mul_f32_e32 v10, v10, v12
	v_bfe_u32 v12, v11, 16, 1
	v_add3_u32 v11, v11, v12, s97
	ds_write_b16_d16_hi v188, v11 offset:12336
	v_bfe_u32 v11, v10, 16, 1
	v_add3_u32 v10, v10, v11, s97
	ds_write_b16_d16_hi v188, v10 offset:49200
	v_mul_f32_e32 v10, 0x3fb8aa3b, v9
	v_exp_f32_e32 v10, v10
	v_mul_f32_e32 v9, 0xbfb8aa3b, v9
	ds_read_u16 v11, v188 offset:13056
	ds_read_u16 v12, v188 offset:13200
	ds_read_u16 v13, v188 offset:13344
	ds_read_u16 v14, v188 offset:13488
	ds_read_u16 v15, v188 offset:14208
	ds_read_u16 v16, v188 offset:14352
	ds_read_u16 v17, v188 offset:14496
	ds_read_u16 v28, v188 offset:14640
	v_exp_f32_e32 v9, v9
	s_waitcnt lgkmcnt(7)
	v_lshlrev_b32_e32 v11, 16, v11
	v_mul_f32_e32 v10, v10, v11
	ds_read_u16 v11, v188 offset:49920
	ds_read_u16 v18, v188 offset:50064
	ds_read_u16 v19, v188 offset:50208
	ds_read_u16 v20, v188 offset:50352
	ds_read_u16 v21, v188 offset:51072
	ds_read_u16 v22, v188 offset:51216
	ds_read_u16 v23, v188 offset:51360
	ds_read_u16 v29, v188 offset:51504
	v_mul_f32_e32 v10, 0x3e000000, v10
	s_waitcnt lgkmcnt(7)
	v_lshlrev_b32_e32 v11, 16, v11
	v_mul_f32_e32 v9, v9, v11
	v_bfe_u32 v11, v10, 16, 1
	v_add3_u32 v10, v10, v11, s97
	ds_write_b16_d16_hi v188, v10 offset:13056
	v_bfe_u32 v10, v9, 16, 1
	v_add3_u32 v9, v9, v10, s97
	ds_write_b16_d16_hi v188, v9 offset:49920
	v_mul_f32_e32 v9, 0x3fb8aa3b, v8
	v_exp_f32_e32 v9, v9
	v_mul_f32_e32 v8, 0xbfb8aa3b, v8
	v_exp_f32_e32 v8, v8
	v_lshlrev_b32_e32 v10, 16, v12
	v_mul_f32_e32 v9, v9, v10
	v_mul_f32_e32 v9, 0x3e000000, v9
	s_waitcnt lgkmcnt(8)
	v_lshlrev_b32_e32 v10, 16, v18
	v_mul_f32_e32 v8, v8, v10
	v_bfe_u32 v10, v9, 16, 1
	v_add3_u32 v9, v9, v10, s97
	ds_write_b16_d16_hi v188, v9 offset:13200
	v_bfe_u32 v9, v8, 16, 1
	v_add3_u32 v8, v8, v9, s97
	ds_write_b16_d16_hi v188, v8 offset:50064
	v_mul_f32_e32 v8, 0x3fb8aa3b, v7
	v_exp_f32_e32 v8, v8
	v_mul_f32_e32 v7, 0xbfb8aa3b, v7
	v_exp_f32_e32 v7, v7
	v_lshlrev_b32_e32 v9, 16, v13
	v_mul_f32_e32 v8, v8, v9
	v_mul_f32_e32 v8, 0x3e000000, v8
	s_waitcnt lgkmcnt(9)
	v_lshlrev_b32_e32 v9, 16, v19
	v_mul_f32_e32 v7, v7, v9
	v_bfe_u32 v9, v8, 16, 1
	v_add3_u32 v8, v8, v9, s97
	ds_write_b16_d16_hi v188, v8 offset:13344
	v_bfe_u32 v8, v7, 16, 1
	v_add3_u32 v7, v7, v8, s97
	ds_write_b16_d16_hi v188, v7 offset:50208
	v_mul_f32_e32 v7, 0x3fb8aa3b, v6
	v_exp_f32_e32 v7, v7
	v_mul_f32_e32 v6, 0xbfb8aa3b, v6
	v_exp_f32_e32 v6, v6
	v_lshlrev_b32_e32 v8, 16, v14
	v_mul_f32_e32 v7, v7, v8
	v_mul_f32_e32 v7, 0x3e000000, v7
	s_waitcnt lgkmcnt(10)
	v_lshlrev_b32_e32 v8, 16, v20
	v_mul_f32_e32 v6, v6, v8
	v_bfe_u32 v8, v7, 16, 1
	v_add3_u32 v7, v7, v8, s97
	ds_write_b16_d16_hi v188, v7 offset:13488
	v_bfe_u32 v7, v6, 16, 1
	v_add3_u32 v6, v6, v7, s97
	ds_write_b16_d16_hi v188, v6 offset:50352
	v_mul_f32_e32 v6, 0x3fb8aa3b, v5
	v_exp_f32_e32 v6, v6
	v_mul_f32_e32 v5, 0xbfb8aa3b, v5
	v_exp_f32_e32 v5, v5
	v_lshlrev_b32_e32 v7, 16, v15
	v_mul_f32_e32 v6, v6, v7
	v_mul_f32_e32 v6, 0x3e000000, v6
	s_waitcnt lgkmcnt(11)
	v_lshlrev_b32_e32 v7, 16, v21
	v_mul_f32_e32 v5, v5, v7
	v_bfe_u32 v7, v6, 16, 1
	v_add3_u32 v6, v6, v7, s97
	ds_write_b16_d16_hi v188, v6 offset:14208
	v_bfe_u32 v6, v5, 16, 1
	v_add3_u32 v5, v5, v6, s97
	ds_write_b16_d16_hi v188, v5 offset:51072
	v_mul_f32_e32 v5, 0x3fb8aa3b, v4
	v_exp_f32_e32 v9, v5
	v_mul_f32_e32 v4, 0xbfb8aa3b, v4
	v_exp_f32_e32 v10, v4
	v_lshlrev_b32_e32 v8, 16, v16
	v_mul_f32_e32 v8, v9, v8
	s_waitcnt lgkmcnt(12)
	v_lshlrev_b32_e32 v9, 16, v22
	s_lshl_b32 s0, s74, 2
	v_mul_f32_e32 v12, v10, v9
	s_add_i32 s0, s0, s49
	v_bfe_u32 v13, v12, 16, 1
	s_ashr_i32 s1, s0, 31
	v_add3_u32 v12, v12, v13, s97
	s_lshl_b64 s[0:1], s[0:1], 14
	ds_write_b16_d16_hi v188, v12 offset:51216
	v_mul_f32_e32 v12, 0x3fb8aa3b, v3
	v_lshl_add_u64 v[32:33], v[142:143], 0, s[0:1]
	v_lshlrev_b32_e32 v16, 16, v17
	v_exp_f32_e32 v17, v12
	global_load_dwordx4 v[4:7], v[32:33], off
	v_mul_f32_e32 v3, 0xbfb8aa3b, v3
	v_exp_f32_e32 v3, v3
	v_mul_f32_e32 v16, v17, v16
	v_mul_f32_e32 v16, 0x3e000000, v16
	s_waitcnt lgkmcnt(12)
	v_lshlrev_b32_e32 v17, 16, v23
	v_mul_f32_e32 v8, 0x3e000000, v8
	v_mul_f32_e32 v3, v3, v17
	v_bfe_u32 v17, v16, 16, 1
	s_movk_i32 s0, 0x2000
	v_bfe_u32 v9, v8, 16, 1
	v_add3_u32 v20, v16, v17, s97
	v_add_co_u32_e32 v34, vcc, s0, v32
	v_add3_u32 v8, v8, v9, s97
	ds_write_b16_d16_hi v188, v20 offset:14496
	v_bfe_u32 v20, v3, 16, 1
	v_addc_co_u32_e32 v35, vcc, 0, v33, vcc
	ds_write_b16_d16_hi v188, v8 offset:14352
	global_load_dwordx4 v[8:11], v[32:33], off offset:32
	v_add3_u32 v3, v3, v20, s97
	global_load_dwordx4 v[20:23], v[34:35], off offset:-4096
	v_add_co_u32_e32 v36, vcc, s83, v32
	global_load_dwordx4 v[12:15], v[32:33], off offset:64
	global_load_dwordx4 v[16:19], v[32:33], off offset:96
	v_addc_co_u32_e32 v37, vcc, 0, v33, vcc
	global_load_dwordx4 v[24:27], v[36:37], off offset:32
	ds_write_b16_d16_hi v188, v3 offset:51360
	v_mul_f32_e32 v3, 0x3fb8aa3b, v2
	v_exp_f32_e32 v3, v3
	v_mul_f32_e32 v2, 0xbfb8aa3b, v2
	v_exp_f32_e32 v2, v2
	v_lshlrev_b32_e32 v28, 16, v28
	v_mul_f32_e32 v3, v3, v28
	s_waitcnt lgkmcnt(14)
	v_lshlrev_b32_e32 v28, 16, v29
	v_mul_f32_e32 v2, v2, v28
	global_load_dwordx4 v[28:31], v[36:37], off offset:64
	v_mul_f32_e32 v3, 0x3e000000, v3
	v_bfe_u32 v38, v3, 16, 1
	v_add3_u32 v3, v3, v38, s97
	ds_write_b16_d16_hi v188, v3 offset:14640
	v_bfe_u32 v3, v2, 16, 1
	v_add3_u32 v2, v2, v3, s97
	ds_write_b16_d16_hi v188, v2 offset:51504
	global_load_dwordx4 v[66:69], v[36:37], off offset:96
	global_load_dwordx4 v[70:73], v[34:35], off
	global_load_dwordx4 v[232:235], v[34:35], off offset:32
	global_load_dwordx4 v[236:239], v[34:35], off offset:64
	global_load_dwordx4 v[240:243], v[34:35], off offset:96
	s_movk_i32 s0, 0x3000
	v_add_co_u32_e32 v2, vcc, s0, v32
	s_mov_b32 s0, 0
	s_nop 0
	v_addc_co_u32_e32 v3, vcc, 0, v33, vcc
	global_load_dwordx4 v[244:247], v[2:3], off
	global_load_dwordx4 v[248:251], v[2:3], off offset:32
	global_load_dwordx4 v[208:211], v[2:3], off offset:64
	global_load_dwordx4 v[212:215], v[2:3], off offset:96
	global_load_dwordx4 v[110:113], v[74:75], off offset:2048
	global_load_dwordx4 v[106:109], v[76:77], off offset:2048
	global_load_dwordx4 v[102:105], v[78:79], off offset:2048
	global_load_dwordx4 v[98:101], v[80:81], off offset:2048
	global_load_dwordx4 v[94:97], v[82:83], off offset:2048
	global_load_dwordx4 v[90:93], v[84:85], off offset:2048
	s_nop 0
	global_load_dwordx4 v[86:89], v[86:87], off offset:2048
	s_nop 0
	global_load_dwordx4 v[82:85], v[114:115], off offset:2048
	s_waitcnt lgkmcnt(0)
	s_barrier
	ds_read_b128 v[114:117], v206 offset:6144
	ds_read_b128 v[118:121], v206 offset:6176
	s_waitcnt vmcnt(23) lgkmcnt(1)
	v_mfma_f32_32x32x16_bf16 v[50:65], v[4:7], v[114:117], 0
	ds_read_b128 v[122:125], v206 offset:6208
	ds_read_b128 v[126:129], v206 offset:6240
	s_waitcnt vmcnt(22) lgkmcnt(2)
	v_mfma_f32_32x32x16_bf16 v[50:65], v[8:11], v[118:121], v[50:65]
	s_waitcnt vmcnt(21)
	v_mfma_f32_32x32x16_bf16 v[34:49], v[20:23], v[114:117], 0
	s_waitcnt vmcnt(20) lgkmcnt(1)
	v_mfma_f32_32x32x16_bf16 v[50:65], v[12:15], v[122:125], v[50:65]
	s_waitcnt vmcnt(18)
	v_mfma_f32_32x32x16_bf16 v[34:49], v[24:27], v[118:121], v[34:49]
	s_waitcnt lgkmcnt(0)
	v_mfma_f32_32x32x16_bf16 v[50:65], v[16:19], v[126:129], v[50:65]
	s_waitcnt vmcnt(17)
	v_mfma_f32_32x32x16_bf16 v[34:49], v[28:31], v[122:125], v[34:49]
	s_waitcnt vmcnt(15)
	v_mfma_f32_32x32x16_bf16 v[18:33], v[70:73], v[114:117], 0
	s_waitcnt vmcnt(11)
	v_mfma_f32_32x32x16_bf16 v[2:17], v[244:247], v[114:117], 0
	v_mfma_f32_32x32x16_bf16 v[18:33], v[232:235], v[118:121], v[18:33]
	v_mov_b32_e32 v232, v205
	s_waitcnt vmcnt(10)
	v_mfma_f32_32x32x16_bf16 v[2:17], v[248:251], v[118:121], v[2:17]
	v_mfma_f32_32x32x16_bf16 v[18:33], v[236:239], v[122:125], v[18:33]
	s_waitcnt vmcnt(9)
	v_mfma_f32_32x32x16_bf16 v[2:17], v[208:211], v[122:125], v[2:17]
	v_mfma_f32_32x32x16_bf16 v[34:49], v[66:69], v[126:129], v[34:49]
	v_mfma_f32_32x32x16_bf16 v[18:33], v[240:243], v[126:129], v[18:33]
	s_waitcnt vmcnt(8)
	v_mfma_f32_32x32x16_bf16 v[2:17], v[212:215], v[126:129], v[2:17]
	s_branch .LBB0_1422
